# v68 with the split-K partials exchanged by system-scope stores and loads instead of L2 writeback / invalidate
# speedup vs baseline: 1.0057x; 1.0006x over previous
; #define PG8_STAGE(bufoff, gbase, voff) do { _Pragma("unroll") for (int _i = 0; _i < 2; ++_i) \
;         __builtin_amdgcn_global_load_lds((const unsigned*)((const char*)(gbase) + (voff)[_i]), (LAS unsigned*)(lds + (bufoff) + ldsw + _i * 8192), 16, 0, 0); } while (0)
; #define PG8_LDA(dst, b, h) do { _Pragma("unroll") for (int m = 0; m < 4; ++m) _Pragma("unroll") for (int k = 0; k < 2; ++k) dst[m][k] = *(const LAS bf16x8*)(lds + PG8_SA(b, h) + aoff + m * 2048 + k * 1024); } while (0)
; #define PG8_LDB(dst, b, h) do { _Pragma("unroll") for (int n = 0; n < 2; ++n) _Pragma("unroll") for (int k = 0; k < 2; ++k) dst[n][k] = *(const LAS bf16x8*)(lds + PG8_SB(b, h) + boff + n * 2048 + k * 1024); } while (0)
; #define PG8_MMA(ai, bj, At, Bt) do { __builtin_amdgcn_s_setprio(1); _Pragma("unroll") for (int m = 0; m < 4; ++m) _Pragma("unroll") for (int n = 0; n < 2; ++n) _Pragma("unroll") for (int k = 0; k < 2; ++k) \
;         acc[ai][bj][m][n] = __builtin_amdgcn_mfma_f32_16x16x32_bf16(Bt[n][k], At[m][k], acc[ai][bj][m][n], 0, 0, 0); __builtin_amdgcn_s_setprio(0); } while (0)
; #define PG8_WAIT_L(n) asm volatile("s_waitcnt lgkmcnt(" #n ")" ::: "memory")
; #define PG8_BAR __builtin_amdgcn_s_barrier()
; template <class Epi>
; __device__ __forceinline__ void gemm_phase(LAS unsigned char* lds, const int tid, const Gemm g, const Sched& S, const Epi& E) {
;     ...
;         const bool has_next = S.next(ui + 1, nxt);
;         const char* nA = has_next ? (const char*)g.A + nxt.aoff : cA; const char* nB = has_next ? (const char*)g.Bt + nxt.boff : cB;
;         for (int t = 0; t < nt; t += 2) {
;             const bool last = (t == nt - 2);
;             const char* a1 = cA + (size_t)(t + 1) * kstA;
;             const char* a2 = last ? nA : cA + (size_t)(t + 2) * kstA; const char* b2 = last ? nB : cB + (size_t)(t + 2) * kstep;
;             const char* a3 = a2 + kstA; const char* b3 = b2 + kstep;
;             PG8_LDB(B0, 0, 0); PG8_SCHED; PG8_LDA(At, 0, 0); PG8_STAGE(PG8_SA(1, 1), a1 + hstepA, voffA);
;             PG8_WAIT_L(8); PG8_BAR; PG8_WAIT_L(0); PG8_MMA(0, 0, At, B0); PG8_BAR; PG8_SCHED;
;             PG8_LDB(B1, 0, 1); PG8_STAGE(PG8_SB(0, 0), b2, voffB);
;             PG8_BAR; PG8_WAIT_L(0); PG8_MMA(0, 1, At, B1); PG8_BAR;
;             PG8_LDA(At, 0, 1); PG8_STAGE(PG8_SA(0, 0), a2, voffA);
;             PG8_BAR; PG8_WAIT_L(0); PG8_MMA(1, 0, At, B0); PG8_BAR; PG8_SCHED;
.LBB0_489:
	s_add_u32 s8, s6, 0xff002000
	s_addc_u32 s9, s7, -1
	s_cmp_eq_u32 s51, 28
	s_cselect_b32 s12, s46, s8
	s_cselect_b32 s13, s42, s9
	s_cselect_b32 s8, s48, s49
	s_cselect_b32 s9, s47, s50
	s_add_u32 s10, s12, 0x2000
	s_addc_u32 s11, s13, 0
	s_add_i32 s52, 0, 0x10000
	v_add_u32_e32 v0, s52, v165
	ds_read_b128 v[46:49], v0
	ds_read_b128 v[54:57], v0 offset:1024
	ds_read_b128 v[138:141], v0 offset:2048
	ds_read_b128 v[158:161], v0 offset:3072
	v_lshl_add_u64 v[162:163], s[6:7], 0, v[154:155]
	s_add_i32 m0, s20, 0xc000
	ds_read_b128 v[168:171], v166
	ds_read_b128 v[172:175], v166 offset:1024
	ds_read_b128 v[176:179], v166 offset:2048
	ds_read_b128 v[180:183], v166 offset:3072
	ds_read_b128 v[196:199], v166 offset:4096
	ds_read_b128 v[200:203], v166 offset:5120
	ds_read_b128 v[204:207], v166 offset:6144
	ds_read_b128 v[208:211], v166 offset:7168
	global_load_lds_dwordx4 v[162:163], off
	v_lshl_add_u64 v[162:163], s[6:7], 0, v[156:157]
	s_add_i32 m0, s20, 0xe000
	s_nop 0
	global_load_lds_dwordx4 v[162:163], off
	s_waitcnt lgkmcnt(8)
	s_barrier
	s_waitcnt lgkmcnt(0)
	s_setprio 1
	s_waitcnt lgkmcnt(0)
	v_mfma_f32_16x16x32_bf16 v[66:69], v[46:49], v[168:171], v[66:69]
	v_mfma_f32_16x16x32_bf16 v[38:41], v[138:141], v[168:171], v[38:41]
	v_mfma_f32_16x16x32_bf16 v[126:129], v[46:49], v[176:179], v[126:129]
	v_mfma_f32_16x16x32_bf16 v[122:125], v[138:141], v[176:179], v[122:125]
	v_mfma_f32_16x16x32_bf16 v[110:113], v[46:49], v[196:199], v[110:113]
	v_mfma_f32_16x16x32_bf16 v[106:109], v[138:141], v[196:199], v[106:109]
	v_mfma_f32_16x16x32_bf16 v[94:97], v[46:49], v[204:207], v[94:97]
	v_mfma_f32_16x16x32_bf16 v[90:93], v[138:141], v[204:207], v[90:93]
	v_mfma_f32_16x16x32_bf16 v[66:69], v[54:57], v[172:175], v[66:69]
	v_mfma_f32_16x16x32_bf16 v[38:41], v[158:161], v[172:175], v[38:41]
	v_mfma_f32_16x16x32_bf16 v[126:129], v[54:57], v[180:183], v[126:129]
	v_mfma_f32_16x16x32_bf16 v[122:125], v[158:161], v[180:183], v[122:125]
	v_mfma_f32_16x16x32_bf16 v[110:113], v[54:57], v[200:203], v[110:113]
	v_mfma_f32_16x16x32_bf16 v[106:109], v[158:161], v[200:203], v[106:109]
	v_mfma_f32_16x16x32_bf16 v[94:97], v[54:57], v[208:211], v[94:97]
	v_mfma_f32_16x16x32_bf16 v[90:93], v[158:161], v[208:211], v[90:93]
	s_setprio 0
	s_barrier
	s_add_i32 s54, 0, 0x14000
	s_add_i32 s52, s52, s17
	v_add_u32_e32 v0, s54, v165
	v_lshl_add_u64 v[162:163], s[8:9], 0, v[144:145]
	s_mov_b32 m0, s52
	ds_read_b128 v[212:215], v0
	ds_read_b128 v[216:219], v0 offset:1024
	ds_read_b128 v[220:223], v0 offset:2048
	ds_read_b128 v[224:227], v0 offset:3072
	global_load_lds_dwordx4 v[162:163], off
	v_lshl_add_u64 v[184:185], s[8:9], 0, v[148:149]
	s_add_i32 m0, s52, 0x2000
	s_nop 0
	global_load_lds_dwordx4 v[184:185], off
	s_barrier
	s_waitcnt lgkmcnt(0)
	s_setprio 1
	s_waitcnt lgkmcnt(0)
	v_mfma_f32_16x16x32_bf16 v[134:137], v[212:215], v[168:171], v[134:137]
	v_mfma_f32_16x16x32_bf16 v[130:133], v[220:223], v[168:171], v[130:133]
	v_mfma_f32_16x16x32_bf16 v[118:121], v[212:215], v[176:179], v[118:121]
	v_mfma_f32_16x16x32_bf16 v[114:117], v[220:223], v[176:179], v[114:117]
	v_mfma_f32_16x16x32_bf16 v[102:105], v[212:215], v[196:199], v[102:105]
	v_mfma_f32_16x16x32_bf16 v[98:101], v[220:223], v[196:199], v[98:101]
	v_mfma_f32_16x16x32_bf16 v[86:89], v[212:215], v[204:207], v[86:89]
	v_mfma_f32_16x16x32_bf16 v[82:85], v[220:223], v[204:207], v[82:85]
	v_mfma_f32_16x16x32_bf16 v[134:137], v[216:219], v[172:175], v[134:137]
	v_mfma_f32_16x16x32_bf16 v[130:133], v[224:227], v[172:175], v[130:133]
	v_mfma_f32_16x16x32_bf16 v[118:121], v[216:219], v[180:183], v[118:121]
	v_mfma_f32_16x16x32_bf16 v[114:117], v[224:227], v[180:183], v[114:117]
	v_mfma_f32_16x16x32_bf16 v[102:105], v[216:219], v[200:203], v[102:105]
	v_mfma_f32_16x16x32_bf16 v[98:101], v[224:227], v[200:203], v[98:101]
	v_mfma_f32_16x16x32_bf16 v[86:89], v[216:219], v[208:211], v[86:89]
	v_mfma_f32_16x16x32_bf16 v[82:85], v[224:227], v[208:211], v[82:85]
	s_setprio 0
	s_mov_b32 m0, s20
	v_lshl_add_u64 v[228:229], s[12:13], 0, v[142:143]
	s_barrier
	ds_read_b128 v[168:171], v166 offset:16384
	ds_read_b128 v[172:175], v166 offset:17408
	ds_read_b128 v[176:179], v166 offset:18432
	ds_read_b128 v[180:183], v166 offset:19456
	ds_read_b128 v[196:199], v166 offset:20480
	ds_read_b128 v[200:203], v166 offset:21504
	ds_read_b128 v[204:207], v166 offset:22528
	ds_read_b128 v[208:211], v166 offset:23552
	global_load_lds_dwordx4 v[228:229], off
	v_lshl_add_u64 v[228:229], s[12:13], 0, v[146:147]
	s_mov_b32 m0, s21
	s_nop 0
	global_load_lds_dwordx4 v[228:229], off
	s_barrier
	s_waitcnt lgkmcnt(0)
	s_setprio 1
	s_waitcnt lgkmcnt(0)
	v_mfma_f32_16x16x32_bf16 v[78:81], v[46:49], v[168:171], v[78:81]
	v_mfma_f32_16x16x32_bf16 v[74:77], v[138:141], v[168:171], v[74:77]
	v_mfma_f32_16x16x32_bf16 v[58:61], v[46:49], v[176:179], v[58:61]
	v_mfma_f32_16x16x32_bf16 v[50:53], v[138:141], v[176:179], v[50:53]
	v_mfma_f32_16x16x32_bf16 v[30:33], v[46:49], v[196:199], v[30:33]
	v_mfma_f32_16x16x32_bf16 v[26:29], v[138:141], v[196:199], v[26:29]
	v_mfma_f32_16x16x32_bf16 v[14:17], v[46:49], v[204:207], v[14:17]
	v_mfma_f32_16x16x32_bf16 v[10:13], v[138:141], v[204:207], v[10:13]
	v_mfma_f32_16x16x32_bf16 v[78:81], v[54:57], v[172:175], v[78:81]
	v_mfma_f32_16x16x32_bf16 v[74:77], v[158:161], v[172:175], v[74:77]
	v_mfma_f32_16x16x32_bf16 v[58:61], v[54:57], v[180:183], v[58:61]
	v_mfma_f32_16x16x32_bf16 v[50:53], v[158:161], v[180:183], v[50:53]
	v_mfma_f32_16x16x32_bf16 v[30:33], v[54:57], v[200:203], v[30:33]
	v_mfma_f32_16x16x32_bf16 v[26:29], v[158:161], v[200:203], v[26:29]
	v_mfma_f32_16x16x32_bf16 v[14:17], v[54:57], v[208:211], v[14:17]
	v_mfma_f32_16x16x32_bf16 v[10:13], v[158:161], v[208:211], v[10:13]
	s_setprio 0
	s_barrier
; #define PG8_STAGE(bufoff, gbase, voff) do { _Pragma("unroll") for (int _i = 0; _i < 2; ++_i) \
;         __builtin_amdgcn_global_load_lds((const unsigned*)((const char*)(gbase) + (voff)[_i]), (LAS unsigned*)(lds + (bufoff) + ldsw + _i * 8192), 16, 0, 0); } while (0)
; #define PG8_LDA(dst, b, h) do { _Pragma("unroll") for (int m = 0; m < 4; ++m) _Pragma("unroll") for (int k = 0; k < 2; ++k) dst[m][k] = *(const LAS bf16x8*)(lds + PG8_SA(b, h) + aoff + m * 2048 + k * 1024); } while (0)
; #define PG8_LDB(dst, b, h) do { _Pragma("unroll") for (int n = 0; n < 2; ++n) _Pragma("unroll") for (int k = 0; k < 2; ++k) dst[n][k] = *(const LAS bf16x8*)(lds + PG8_SB(b, h) + boff + n * 2048 + k * 1024); } while (0)
; #define PG8_MMA(ai, bj, At, Bt) do { __builtin_amdgcn_s_setprio(1); _Pragma("unroll") for (int m = 0; m < 4; ++m) _Pragma("unroll") for (int n = 0; n < 2; ++n) _Pragma("unroll") for (int k = 0; k < 2; ++k) \
;         acc[ai][bj][m][n] = __builtin_amdgcn_mfma_f32_16x16x32_bf16(Bt[n][k], At[m][k], acc[ai][bj][m][n], 0, 0, 0); __builtin_amdgcn_s_setprio(0); } while (0)
; #define PG8_WAIT_V(n) asm volatile("s_waitcnt vmcnt(" #n ")" ::: "memory")
; #define PG8_WAIT_L(n) asm volatile("s_waitcnt lgkmcnt(" #n ")" ::: "memory")
; #define PG8_BAR __builtin_amdgcn_s_barrier()
; #define PG8_SCHED __builtin_amdgcn_sched_barrier(0)
; template <class Epi>
; __device__ __forceinline__ void gemm_phase(LAS unsigned char* lds, const int tid, const Gemm g, const Sched& S, const Epi& E) {
;     ...
;             PG8_STAGE(PG8_SB(0, 1), b2 + hstepB, voffB);
;             PG8_WAIT_V(6); PG8_BAR; PG8_MMA(1, 1, At, B1); PG8_BAR;
;             PG8_LDB(B0, 1, 0); PG8_SCHED; PG8_LDA(At, 1, 0); PG8_STAGE(PG8_SA(0, 1), a2 + hstepA, voffA);
;             PG8_WAIT_L(8); PG8_BAR; PG8_WAIT_L(0); PG8_MMA(0, 0, At, B0); PG8_BAR; PG8_SCHED;
;             PG8_LDB(B1, 1, 1); PG8_STAGE(PG8_SB(1, 0), b3, voffB);
;             PG8_BAR; PG8_WAIT_L(0); PG8_MMA(0, 1, At, B1); PG8_BAR;
;             PG8_LDA(At, 1, 1); PG8_STAGE(PG8_SA(1, 0), a3, voffA);
;             PG8_BAR; PG8_WAIT_L(0); PG8_MMA(1, 0, At, B0); PG8_BAR; PG8_SCHED;
	s_add_u32 s52, s8, 0x80000
	s_addc_u32 s53, s9, 0
	s_add_i32 s54, s54, s17
	v_lshl_add_u64 v[46:47], s[52:53], 0, v[144:145]
	s_mov_b32 m0, s54
	s_nop 0
	global_load_lds_dwordx4 v[46:47], off
	v_lshl_add_u64 v[46:47], s[52:53], 0, v[148:149]
	s_add_i32 m0, s54, 0x2000
	s_nop 0
	global_load_lds_dwordx4 v[46:47], off
	s_waitcnt vmcnt(6)
	s_barrier
	s_setprio 1
	v_mfma_f32_16x16x32_bf16 v[42:45], v[212:215], v[176:179], v[42:45]
	v_mfma_f32_16x16x32_bf16 v[34:37], v[220:223], v[176:179], v[34:37]
	v_mfma_f32_16x16x32_bf16 v[22:25], v[212:215], v[196:199], v[22:25]
	v_mfma_f32_16x16x32_bf16 v[18:21], v[220:223], v[196:199], v[18:21]
	v_mfma_f32_16x16x32_bf16 v[6:9], v[212:215], v[204:207], v[6:9]
	v_mfma_f32_16x16x32_bf16 v[2:5], v[220:223], v[204:207], v[2:5]
	v_mfma_f32_16x16x32_bf16 v[46:49], v[212:215], v[168:171], v[70:73]
	v_mfma_f32_16x16x32_bf16 v[54:57], v[220:223], v[168:171], v[62:65]
	v_mfma_f32_16x16x32_bf16 v[42:45], v[216:219], v[180:183], v[42:45]
	v_mfma_f32_16x16x32_bf16 v[34:37], v[224:227], v[180:183], v[34:37]
	v_mfma_f32_16x16x32_bf16 v[22:25], v[216:219], v[200:203], v[22:25]
	v_mfma_f32_16x16x32_bf16 v[18:21], v[224:227], v[200:203], v[18:21]
	v_mfma_f32_16x16x32_bf16 v[6:9], v[216:219], v[208:211], v[6:9]
	v_mfma_f32_16x16x32_bf16 v[2:5], v[224:227], v[208:211], v[2:5]
	v_mfma_f32_16x16x32_bf16 v[46:49], v[216:219], v[172:175], v[46:49]
	v_mfma_f32_16x16x32_bf16 v[54:57], v[224:227], v[172:175], v[54:57]
	s_setprio 0
	s_add_i32 s52, 0, 0x18000
	v_add_u32_e32 v0, s52, v165
	s_barrier
	ds_read_b128 v[62:65], v0
	ds_read_b128 v[70:73], v0 offset:1024
	ds_read_b128 v[138:141], v0 offset:2048
	ds_read_b128 v[158:161], v0 offset:3072
	s_add_u32 s12, s12, 0x1000000
	s_addc_u32 s13, s13, 0
	s_mov_b32 m0, s26
	v_lshl_add_u64 v[212:213], s[12:13], 0, v[142:143]
	ds_read_b128 v[168:171], v166 offset:32768
	ds_read_b128 v[172:175], v166 offset:33792
	ds_read_b128 v[176:179], v166 offset:34816
	ds_read_b128 v[180:183], v166 offset:35840
	ds_read_b128 v[196:199], v166 offset:36864
	ds_read_b128 v[200:203], v166 offset:37888
	ds_read_b128 v[204:207], v166 offset:38912
	ds_read_b128 v[208:211], v166 offset:39936
	global_load_lds_dwordx4 v[212:213], off
	v_lshl_add_u64 v[212:213], s[12:13], 0, v[146:147]
	s_mov_b32 m0, s27
	s_nop 0
	global_load_lds_dwordx4 v[212:213], off
	s_waitcnt lgkmcnt(8)
	s_barrier
	s_waitcnt lgkmcnt(0)
	s_setprio 1
	s_waitcnt lgkmcnt(0)
	v_mfma_f32_16x16x32_bf16 v[66:69], v[62:65], v[168:171], v[66:69]
	v_mfma_f32_16x16x32_bf16 v[38:41], v[138:141], v[168:171], v[38:41]
	v_mfma_f32_16x16x32_bf16 v[126:129], v[62:65], v[176:179], v[126:129]
	v_mfma_f32_16x16x32_bf16 v[122:125], v[138:141], v[176:179], v[122:125]
	v_mfma_f32_16x16x32_bf16 v[110:113], v[62:65], v[196:199], v[110:113]
	v_mfma_f32_16x16x32_bf16 v[106:109], v[138:141], v[196:199], v[106:109]
	v_mfma_f32_16x16x32_bf16 v[94:97], v[62:65], v[204:207], v[94:97]
	v_mfma_f32_16x16x32_bf16 v[90:93], v[138:141], v[204:207], v[90:93]
	v_mfma_f32_16x16x32_bf16 v[66:69], v[70:73], v[172:175], v[66:69]
	v_mfma_f32_16x16x32_bf16 v[38:41], v[158:161], v[172:175], v[38:41]
	v_mfma_f32_16x16x32_bf16 v[126:129], v[70:73], v[180:183], v[126:129]
	v_mfma_f32_16x16x32_bf16 v[122:125], v[158:161], v[180:183], v[122:125]
	v_mfma_f32_16x16x32_bf16 v[110:113], v[70:73], v[200:203], v[110:113]
	v_mfma_f32_16x16x32_bf16 v[106:109], v[158:161], v[200:203], v[106:109]
	v_mfma_f32_16x16x32_bf16 v[94:97], v[70:73], v[208:211], v[94:97]
	v_mfma_f32_16x16x32_bf16 v[90:93], v[158:161], v[208:211], v[90:93]
	s_setprio 0
	s_barrier
	s_add_i32 s12, 0, 0x1c000
	s_add_i32 s13, s52, s17
	v_add_u32_e32 v0, s12, v165
	v_lshl_add_u64 v[162:163], v[162:163], 0, s[44:45]
	s_mov_b32 m0, s13
	ds_read_b128 v[212:215], v0
	ds_read_b128 v[216:219], v0 offset:1024
	ds_read_b128 v[220:223], v0 offset:2048
	ds_read_b128 v[224:227], v0 offset:3072
	global_load_lds_dwordx4 v[162:163], off
	v_lshl_add_u64 v[162:163], v[184:185], 0, s[44:45]
	s_add_i32 m0, s13, 0x2000
	s_nop 0
	global_load_lds_dwordx4 v[162:163], off
	s_barrier
	s_waitcnt lgkmcnt(0)
	s_setprio 1
	s_waitcnt lgkmcnt(0)
	v_mfma_f32_16x16x32_bf16 v[134:137], v[212:215], v[168:171], v[134:137]
	v_mfma_f32_16x16x32_bf16 v[130:133], v[220:223], v[168:171], v[130:133]
	v_mfma_f32_16x16x32_bf16 v[118:121], v[212:215], v[176:179], v[118:121]
	v_mfma_f32_16x16x32_bf16 v[114:117], v[220:223], v[176:179], v[114:117]
	v_mfma_f32_16x16x32_bf16 v[102:105], v[212:215], v[196:199], v[102:105]
	v_mfma_f32_16x16x32_bf16 v[98:101], v[220:223], v[196:199], v[98:101]
	v_mfma_f32_16x16x32_bf16 v[86:89], v[212:215], v[204:207], v[86:89]
	v_mfma_f32_16x16x32_bf16 v[82:85], v[220:223], v[204:207], v[82:85]
	v_mfma_f32_16x16x32_bf16 v[134:137], v[216:219], v[172:175], v[134:137]
	v_mfma_f32_16x16x32_bf16 v[130:133], v[224:227], v[172:175], v[130:133]
	v_mfma_f32_16x16x32_bf16 v[118:121], v[216:219], v[180:183], v[118:121]
	v_mfma_f32_16x16x32_bf16 v[114:117], v[224:227], v[180:183], v[114:117]
	v_mfma_f32_16x16x32_bf16 v[102:105], v[216:219], v[200:203], v[102:105]
	v_mfma_f32_16x16x32_bf16 v[98:101], v[224:227], v[200:203], v[98:101]
	v_mfma_f32_16x16x32_bf16 v[86:89], v[216:219], v[208:211], v[86:89]
	v_mfma_f32_16x16x32_bf16 v[82:85], v[224:227], v[208:211], v[82:85]
	s_setprio 0
	s_mov_b32 m0, s28
	v_lshl_add_u64 v[162:163], s[10:11], 0, v[142:143]
	s_barrier
	ds_read_b128 v[168:171], v166 offset:49152
	ds_read_b128 v[172:175], v166 offset:50176
	ds_read_b128 v[176:179], v166 offset:51200
	ds_read_b128 v[180:183], v166 offset:52224
	ds_read_b128 v[196:199], v166 offset:53248
	ds_read_b128 v[200:203], v166 offset:54272
	ds_read_b128 v[204:207], v166 offset:55296
	ds_read_b128 v[208:211], v166 offset:56320
	global_load_lds_dwordx4 v[162:163], off
	v_lshl_add_u64 v[162:163], s[10:11], 0, v[146:147]
	s_mov_b32 m0, s29
	s_nop 0
	global_load_lds_dwordx4 v[162:163], off
	s_barrier
; #define PG8_STAGE(bufoff, gbase, voff) do { _Pragma("unroll") for (int _i = 0; _i < 2; ++_i) \
;         __builtin_amdgcn_global_load_lds((const unsigned*)((const char*)(gbase) + (voff)[_i]), (LAS unsigned*)(lds + (bufoff) + ldsw + _i * 8192), 16, 0, 0); } while (0)
; #define PG8_LDA(dst, b, h) do { _Pragma("unroll") for (int m = 0; m < 4; ++m) _Pragma("unroll") for (int k = 0; k < 2; ++k) dst[m][k] = *(const LAS bf16x8*)(lds + PG8_SA(b, h) + aoff + m * 2048 + k * 1024); } while (0)
; #define PG8_LDB(dst, b, h) do { _Pragma("unroll") for (int n = 0; n < 2; ++n) _Pragma("unroll") for (int k = 0; k < 2; ++k) dst[n][k] = *(const LAS bf16x8*)(lds + PG8_SB(b, h) + boff + n * 2048 + k * 1024); } while (0)
; #define PG8_MMA(ai, bj, At, Bt) do { __builtin_amdgcn_s_setprio(1); _Pragma("unroll") for (int m = 0; m < 4; ++m) _Pragma("unroll") for (int n = 0; n < 2; ++n) _Pragma("unroll") for (int k = 0; k < 2; ++k) \
;         acc[ai][bj][m][n] = __builtin_amdgcn_mfma_f32_16x16x32_bf16(Bt[n][k], At[m][k], acc[ai][bj][m][n], 0, 0, 0); __builtin_amdgcn_s_setprio(0); } while (0)
; #define PG8_WAIT_V(n) asm volatile("s_waitcnt vmcnt(" #n ")" ::: "memory")
; #define PG8_WAIT_L(n) asm volatile("s_waitcnt lgkmcnt(" #n ")" ::: "memory")
; #define PG8_BAR __builtin_amdgcn_s_barrier()
; #define PG8_SCHED __builtin_amdgcn_sched_barrier(0)
; template <class Epi>
; __device__ __forceinline__ void gemm_phase(LAS unsigned char* lds, const int tid, const Gemm g, const Sched& S, const Epi& E) {
;     ...
;             PG8_WAIT_V(6); PG8_BAR; PG8_MMA(1, 1, At, B1); PG8_BAR;
;             PG8_LDB(B0, 1, 0); PG8_SCHED; PG8_LDA(At, 1, 0); PG8_STAGE(PG8_SA(0, 1), a2 + hstepA, voffA);
;             PG8_WAIT_L(8); PG8_BAR; PG8_WAIT_L(0); PG8_MMA(0, 0, At, B0); PG8_BAR; PG8_SCHED;
;             PG8_LDB(B1, 1, 1); PG8_STAGE(PG8_SB(1, 0), b3, voffB);
;             PG8_BAR; PG8_WAIT_L(0); PG8_MMA(0, 1, At, B1); PG8_BAR;
;             PG8_LDA(At, 1, 1); PG8_STAGE(PG8_SA(1, 0), a3, voffA);
;             PG8_BAR; PG8_WAIT_L(0); PG8_MMA(1, 0, At, B0); PG8_BAR; PG8_SCHED;
;             PG8_STAGE(PG8_SB(1, 1), b3 + hstepB, voffB);
;             PG8_WAIT_V(6); PG8_BAR; PG8_MMA(1, 1, At, B1); PG8_BAR;
;         }
;         bool keep = false;
;         if constexpr (!epi_after_drain<Epi>::value) keep = E(acc, cur, wr, wc, fr, fq);
	s_waitcnt lgkmcnt(0)
	s_setprio 1
	s_waitcnt lgkmcnt(0)
	v_mfma_f32_16x16x32_bf16 v[78:81], v[62:65], v[168:171], v[78:81]
	v_mfma_f32_16x16x32_bf16 v[74:77], v[138:141], v[168:171], v[74:77]
	v_mfma_f32_16x16x32_bf16 v[58:61], v[62:65], v[176:179], v[58:61]
	v_mfma_f32_16x16x32_bf16 v[50:53], v[138:141], v[176:179], v[50:53]
	v_mfma_f32_16x16x32_bf16 v[30:33], v[62:65], v[196:199], v[30:33]
	v_mfma_f32_16x16x32_bf16 v[26:29], v[138:141], v[196:199], v[26:29]
	v_mfma_f32_16x16x32_bf16 v[14:17], v[62:65], v[204:207], v[14:17]
	v_mfma_f32_16x16x32_bf16 v[10:13], v[138:141], v[204:207], v[10:13]
	v_mfma_f32_16x16x32_bf16 v[78:81], v[70:73], v[172:175], v[78:81]
	v_mfma_f32_16x16x32_bf16 v[74:77], v[158:161], v[172:175], v[74:77]
	v_mfma_f32_16x16x32_bf16 v[58:61], v[70:73], v[180:183], v[58:61]
	v_mfma_f32_16x16x32_bf16 v[50:53], v[158:161], v[180:183], v[50:53]
	v_mfma_f32_16x16x32_bf16 v[30:33], v[70:73], v[200:203], v[30:33]
	v_mfma_f32_16x16x32_bf16 v[26:29], v[158:161], v[200:203], v[26:29]
	v_mfma_f32_16x16x32_bf16 v[14:17], v[70:73], v[208:211], v[14:17]
	v_mfma_f32_16x16x32_bf16 v[10:13], v[158:161], v[208:211], v[10:13]
	s_setprio 0
	s_barrier
	s_add_u32 s8, s8, 0x80080
	s_addc_u32 s9, s9, 0
	s_add_i32 s10, s12, s17
	v_lshl_add_u64 v[62:63], s[8:9], 0, v[144:145]
	s_mov_b32 m0, s10
	s_nop 0
	global_load_lds_dwordx4 v[62:63], off
	v_lshl_add_u64 v[62:63], s[8:9], 0, v[148:149]
	s_add_i32 m0, s10, 0x2000
	s_nop 0
	global_load_lds_dwordx4 v[62:63], off
	s_waitcnt vmcnt(6)
	s_barrier
	s_setprio 1
	v_mfma_f32_16x16x32_bf16 v[46:49], v[212:215], v[168:171], v[46:49]
	v_mfma_f32_16x16x32_bf16 v[70:73], v[216:219], v[172:175], v[46:49]
	v_mfma_f32_16x16x32_bf16 v[46:49], v[220:223], v[168:171], v[54:57]
	v_mfma_f32_16x16x32_bf16 v[42:45], v[212:215], v[176:179], v[42:45]
	v_mfma_f32_16x16x32_bf16 v[34:37], v[220:223], v[176:179], v[34:37]
	v_mfma_f32_16x16x32_bf16 v[22:25], v[212:215], v[196:199], v[22:25]
	v_mfma_f32_16x16x32_bf16 v[18:21], v[220:223], v[196:199], v[18:21]
	v_mfma_f32_16x16x32_bf16 v[6:9], v[212:215], v[204:207], v[6:9]
	v_mfma_f32_16x16x32_bf16 v[2:5], v[220:223], v[204:207], v[2:5]
	v_mfma_f32_16x16x32_bf16 v[62:65], v[224:227], v[172:175], v[46:49]
	v_mfma_f32_16x16x32_bf16 v[42:45], v[216:219], v[180:183], v[42:45]
	v_mfma_f32_16x16x32_bf16 v[34:37], v[224:227], v[180:183], v[34:37]
	v_mfma_f32_16x16x32_bf16 v[22:25], v[216:219], v[200:203], v[22:25]
	v_mfma_f32_16x16x32_bf16 v[18:21], v[224:227], v[200:203], v[18:21]
	v_mfma_f32_16x16x32_bf16 v[6:9], v[216:219], v[208:211], v[6:9]
	v_mfma_f32_16x16x32_bf16 v[2:5], v[224:227], v[208:211], v[2:5]
	s_setprio 0
	s_add_i32 s51, s51, 2
	s_add_u32 s49, s49, 0x100
	s_addc_u32 s50, s50, 0
	s_add_u32 s6, s6, 0x4000
	s_addc_u32 s7, s7, 0
	s_cmp_gt_u32 s51, 29
	s_barrier
	s_cbranch_scc0 .LBB0_489
	v_readlane_b32 s6, v251, 0
	s_cmp_lt_u32 s6, 16
	s_cbranch_scc1 .Lsk_A
	v_readlane_b32 s8, v253, 52
	v_readlane_b32 s9, v253, 53
	s_and_b32 s6, s6, 15
	s_lshl_b32 s6, s6, 18
	s_add_u32 s8, s8, s6
	s_addc_u32 s9, s9, 0
	s_add_u32 s8, s8, 0x1af00000
	s_addc_u32 s9, s9, 0
	v_lshlrev_b32_e32 v158, 4, v151
	global_store_dwordx4 v158, v[2:5], s[8:9] sc0 sc1
	s_add_u32 s8, s8, 0x2000
	s_addc_u32 s9, s9, 0
	global_store_dwordx4 v158, v[6:9], s[8:9] sc0 sc1
	s_add_u32 s8, s8, 0x2000
	s_addc_u32 s9, s9, 0
	global_store_dwordx4 v158, v[10:13], s[8:9] sc0 sc1
	s_add_u32 s8, s8, 0x2000
	s_addc_u32 s9, s9, 0
	global_store_dwordx4 v158, v[14:17], s[8:9] sc0 sc1
	s_add_u32 s8, s8, 0x2000
	s_addc_u32 s9, s9, 0
	global_store_dwordx4 v158, v[18:21], s[8:9] sc0 sc1
	s_add_u32 s8, s8, 0x2000
	s_addc_u32 s9, s9, 0
	global_store_dwordx4 v158, v[22:25], s[8:9] sc0 sc1
	s_add_u32 s8, s8, 0x2000
	s_addc_u32 s9, s9, 0
	global_store_dwordx4 v158, v[26:29], s[8:9] sc0 sc1
	s_add_u32 s8, s8, 0x2000
	s_addc_u32 s9, s9, 0
	global_store_dwordx4 v158, v[30:33], s[8:9] sc0 sc1
	s_add_u32 s8, s8, 0x2000
	s_addc_u32 s9, s9, 0
	global_store_dwordx4 v158, v[34:37], s[8:9] sc0 sc1
	s_add_u32 s8, s8, 0x2000
	s_addc_u32 s9, s9, 0
	global_store_dwordx4 v158, v[38:41], s[8:9] sc0 sc1
	s_add_u32 s8, s8, 0x2000
	s_addc_u32 s9, s9, 0
	global_store_dwordx4 v158, v[42:45], s[8:9] sc0 sc1
	s_add_u32 s8, s8, 0x2000
	s_addc_u32 s9, s9, 0
	global_store_dwordx4 v158, v[50:53], s[8:9] sc0 sc1
	s_add_u32 s8, s8, 0x2000
	s_addc_u32 s9, s9, 0
	global_store_dwordx4 v158, v[58:61], s[8:9] sc0 sc1
	s_add_u32 s8, s8, 0x2000
	s_addc_u32 s9, s9, 0
	global_store_dwordx4 v158, v[62:65], s[8:9] sc0 sc1
	s_add_u32 s8, s8, 0x2000
	s_addc_u32 s9, s9, 0
	global_store_dwordx4 v158, v[66:69], s[8:9] sc0 sc1
	s_add_u32 s8, s8, 0x2000
	s_addc_u32 s9, s9, 0
	global_store_dwordx4 v158, v[70:73], s[8:9] sc0 sc1
	s_add_u32 s8, s8, 0x2000
	s_addc_u32 s9, s9, 0
	global_store_dwordx4 v158, v[74:77], s[8:9] sc0 sc1
	s_add_u32 s8, s8, 0x2000
	s_addc_u32 s9, s9, 0
	global_store_dwordx4 v158, v[78:81], s[8:9] sc0 sc1
	s_add_u32 s8, s8, 0x2000
	s_addc_u32 s9, s9, 0
	global_store_dwordx4 v158, v[82:85], s[8:9] sc0 sc1
	s_add_u32 s8, s8, 0x2000
	s_addc_u32 s9, s9, 0
	global_store_dwordx4 v158, v[86:89], s[8:9] sc0 sc1
	s_add_u32 s8, s8, 0x2000
	s_addc_u32 s9, s9, 0
	global_store_dwordx4 v158, v[90:93], s[8:9] sc0 sc1
	s_add_u32 s8, s8, 0x2000
	s_addc_u32 s9, s9, 0
	global_store_dwordx4 v158, v[94:97], s[8:9] sc0 sc1
	s_add_u32 s8, s8, 0x2000
	s_addc_u32 s9, s9, 0
	global_store_dwordx4 v158, v[98:101], s[8:9] sc0 sc1
	s_add_u32 s8, s8, 0x2000
	s_addc_u32 s9, s9, 0
	global_store_dwordx4 v158, v[102:105], s[8:9] sc0 sc1
	s_add_u32 s8, s8, 0x2000
	s_addc_u32 s9, s9, 0
	global_store_dwordx4 v158, v[106:109], s[8:9] sc0 sc1
	s_add_u32 s8, s8, 0x2000
	s_addc_u32 s9, s9, 0
	global_store_dwordx4 v158, v[110:113], s[8:9] sc0 sc1
	s_add_u32 s8, s8, 0x2000
	s_addc_u32 s9, s9, 0
	global_store_dwordx4 v158, v[114:117], s[8:9] sc0 sc1
	s_add_u32 s8, s8, 0x2000
	s_addc_u32 s9, s9, 0
	global_store_dwordx4 v158, v[118:121], s[8:9] sc0 sc1
	s_add_u32 s8, s8, 0x2000
	s_addc_u32 s9, s9, 0
	global_store_dwordx4 v158, v[122:125], s[8:9] sc0 sc1
	s_add_u32 s8, s8, 0x2000
	s_addc_u32 s9, s9, 0
	global_store_dwordx4 v158, v[126:129], s[8:9] sc0 sc1
	s_add_u32 s8, s8, 0x2000
	s_addc_u32 s9, s9, 0
	global_store_dwordx4 v158, v[130:133], s[8:9] sc0 sc1
	s_add_u32 s8, s8, 0x2000
	s_addc_u32 s9, s9, 0
	global_store_dwordx4 v158, v[134:137], s[8:9] sc0 sc1
	s_waitcnt vmcnt(0)
	s_branch .Lsk_bdone

; template <class Epi>
; __device__ __forceinline__ void gemm_phase(LAS unsigned char* lds, const int tid, const Gemm g, const Sched& S, const Epi& E) {
;     ...
;         bool keep = false;
;         if constexpr (!epi_after_drain<Epi>::value) keep = E(acc, cur, wr, wc, fr, fq);
.Lsk_go:
	s_mov_b64 exec, s[6:7]
	global_load_dwordx4 v[196:199], v158, s[8:9] sc0 sc1
	s_add_u32 s8, s8, 0x2000
	s_addc_u32 s9, s9, 0
	global_load_dwordx4 v[200:203], v158, s[8:9] sc0 sc1
	s_add_u32 s8, s8, 0x2000
	s_addc_u32 s9, s9, 0
	global_load_dwordx4 v[204:207], v158, s[8:9] sc0 sc1
	s_add_u32 s8, s8, 0x2000
	s_addc_u32 s9, s9, 0
	global_load_dwordx4 v[208:211], v158, s[8:9] sc0 sc1
	s_add_u32 s8, s8, 0x2000
	s_addc_u32 s9, s9, 0
	global_load_dwordx4 v[212:215], v158, s[8:9] sc0 sc1
	s_add_u32 s8, s8, 0x2000
	s_addc_u32 s9, s9, 0
	global_load_dwordx4 v[46:49], v158, s[8:9] sc0 sc1
	s_add_u32 s8, s8, 0x2000
	s_addc_u32 s9, s9, 0
	global_load_dwordx4 v[54:57], v158, s[8:9] sc0 sc1
	s_add_u32 s8, s8, 0x2000
	s_addc_u32 s9, s9, 0
	global_load_dwordx4 v[138:141], v158, s[8:9] sc0 sc1
	s_add_u32 s8, s8, 0x2000
	s_addc_u32 s9, s9, 0
	s_waitcnt vmcnt(7)
	v_pk_add_f32 v[2:3], v[2:3], v[196:197]
	v_pk_add_f32 v[4:5], v[4:5], v[198:199]
	s_waitcnt vmcnt(6)
	v_pk_add_f32 v[6:7], v[6:7], v[200:201]
	v_pk_add_f32 v[8:9], v[8:9], v[202:203]
	s_waitcnt vmcnt(5)
	v_pk_add_f32 v[10:11], v[10:11], v[204:205]
	v_pk_add_f32 v[12:13], v[12:13], v[206:207]
	s_waitcnt vmcnt(4)
	v_pk_add_f32 v[14:15], v[14:15], v[208:209]
	v_pk_add_f32 v[16:17], v[16:17], v[210:211]
	s_waitcnt vmcnt(3)
	v_pk_add_f32 v[18:19], v[18:19], v[212:213]
	v_pk_add_f32 v[20:21], v[20:21], v[214:215]
	s_waitcnt vmcnt(2)
	v_pk_add_f32 v[22:23], v[22:23], v[46:47]
	v_pk_add_f32 v[24:25], v[24:25], v[48:49]
	s_waitcnt vmcnt(1)
	v_pk_add_f32 v[26:27], v[26:27], v[54:55]
	v_pk_add_f32 v[28:29], v[28:29], v[56:57]
	s_waitcnt vmcnt(0)
	v_pk_add_f32 v[30:31], v[30:31], v[138:139]
	v_pk_add_f32 v[32:33], v[32:33], v[140:141]
	global_load_dwordx4 v[196:199], v158, s[8:9] sc0 sc1
	s_add_u32 s8, s8, 0x2000
	s_addc_u32 s9, s9, 0
	global_load_dwordx4 v[200:203], v158, s[8:9] sc0 sc1
	s_add_u32 s8, s8, 0x2000
	s_addc_u32 s9, s9, 0
	global_load_dwordx4 v[204:207], v158, s[8:9] sc0 sc1
	s_add_u32 s8, s8, 0x2000
	s_addc_u32 s9, s9, 0
	global_load_dwordx4 v[208:211], v158, s[8:9] sc0 sc1
	s_add_u32 s8, s8, 0x2000
	s_addc_u32 s9, s9, 0
	global_load_dwordx4 v[212:215], v158, s[8:9] sc0 sc1
	s_add_u32 s8, s8, 0x2000
	s_addc_u32 s9, s9, 0
	global_load_dwordx4 v[46:49], v158, s[8:9] sc0 sc1
	s_add_u32 s8, s8, 0x2000
	s_addc_u32 s9, s9, 0
	global_load_dwordx4 v[54:57], v158, s[8:9] sc0 sc1
	s_add_u32 s8, s8, 0x2000
	s_addc_u32 s9, s9, 0
	global_load_dwordx4 v[138:141], v158, s[8:9] sc0 sc1
	s_add_u32 s8, s8, 0x2000
	s_addc_u32 s9, s9, 0
	s_waitcnt vmcnt(7)
	v_pk_add_f32 v[34:35], v[34:35], v[196:197]
	v_pk_add_f32 v[36:37], v[36:37], v[198:199]
	s_waitcnt vmcnt(6)
	v_pk_add_f32 v[38:39], v[38:39], v[200:201]
	v_pk_add_f32 v[40:41], v[40:41], v[202:203]
	s_waitcnt vmcnt(5)
	v_pk_add_f32 v[42:43], v[42:43], v[204:205]
	v_pk_add_f32 v[44:45], v[44:45], v[206:207]
	s_waitcnt vmcnt(4)
	v_pk_add_f32 v[50:51], v[50:51], v[208:209]
	v_pk_add_f32 v[52:53], v[52:53], v[210:211]
	s_waitcnt vmcnt(3)
	v_pk_add_f32 v[58:59], v[58:59], v[212:213]
	v_pk_add_f32 v[60:61], v[60:61], v[214:215]
	s_waitcnt vmcnt(2)
	v_pk_add_f32 v[62:63], v[62:63], v[46:47]
	v_pk_add_f32 v[64:65], v[64:65], v[48:49]
	s_waitcnt vmcnt(1)
	v_pk_add_f32 v[66:67], v[66:67], v[54:55]
	v_pk_add_f32 v[68:69], v[68:69], v[56:57]
	s_waitcnt vmcnt(0)
	v_pk_add_f32 v[70:71], v[70:71], v[138:139]
	v_pk_add_f32 v[72:73], v[72:73], v[140:141]
	global_load_dwordx4 v[196:199], v158, s[8:9] sc0 sc1
	s_add_u32 s8, s8, 0x2000
	s_addc_u32 s9, s9, 0
	global_load_dwordx4 v[200:203], v158, s[8:9] sc0 sc1
	s_add_u32 s8, s8, 0x2000
	s_addc_u32 s9, s9, 0
	global_load_dwordx4 v[204:207], v158, s[8:9] sc0 sc1
	s_add_u32 s8, s8, 0x2000
	s_addc_u32 s9, s9, 0
	global_load_dwordx4 v[208:211], v158, s[8:9] sc0 sc1
	s_add_u32 s8, s8, 0x2000
	s_addc_u32 s9, s9, 0
	global_load_dwordx4 v[212:215], v158, s[8:9] sc0 sc1
	s_add_u32 s8, s8, 0x2000
	s_addc_u32 s9, s9, 0
	global_load_dwordx4 v[46:49], v158, s[8:9] sc0 sc1
	s_add_u32 s8, s8, 0x2000
	s_addc_u32 s9, s9, 0
	global_load_dwordx4 v[54:57], v158, s[8:9] sc0 sc1
	s_add_u32 s8, s8, 0x2000
	s_addc_u32 s9, s9, 0
	global_load_dwordx4 v[138:141], v158, s[8:9] sc0 sc1
	s_add_u32 s8, s8, 0x2000
	s_addc_u32 s9, s9, 0
	s_waitcnt vmcnt(7)
	v_pk_add_f32 v[74:75], v[74:75], v[196:197]
	v_pk_add_f32 v[76:77], v[76:77], v[198:199]
	s_waitcnt vmcnt(6)
	v_pk_add_f32 v[78:79], v[78:79], v[200:201]
	v_pk_add_f32 v[80:81], v[80:81], v[202:203]
	s_waitcnt vmcnt(5)
	v_pk_add_f32 v[82:83], v[82:83], v[204:205]
	v_pk_add_f32 v[84:85], v[84:85], v[206:207]
	s_waitcnt vmcnt(4)
	v_pk_add_f32 v[86:87], v[86:87], v[208:209]
	v_pk_add_f32 v[88:89], v[88:89], v[210:211]
	s_waitcnt vmcnt(3)
	v_pk_add_f32 v[90:91], v[90:91], v[212:213]
	v_pk_add_f32 v[92:93], v[92:93], v[214:215]
	s_waitcnt vmcnt(2)
	v_pk_add_f32 v[94:95], v[94:95], v[46:47]
	v_pk_add_f32 v[96:97], v[96:97], v[48:49]
	s_waitcnt vmcnt(1)
	v_pk_add_f32 v[98:99], v[98:99], v[54:55]
	v_pk_add_f32 v[100:101], v[100:101], v[56:57]
	s_waitcnt vmcnt(0)
	v_pk_add_f32 v[102:103], v[102:103], v[138:139]
	v_pk_add_f32 v[104:105], v[104:105], v[140:141]
	global_load_dwordx4 v[196:199], v158, s[8:9] sc0 sc1
	s_add_u32 s8, s8, 0x2000
	s_addc_u32 s9, s9, 0
	global_load_dwordx4 v[200:203], v158, s[8:9] sc0 sc1
	s_add_u32 s8, s8, 0x2000
	s_addc_u32 s9, s9, 0
	global_load_dwordx4 v[204:207], v158, s[8:9] sc0 sc1
	s_add_u32 s8, s8, 0x2000
	s_addc_u32 s9, s9, 0
	global_load_dwordx4 v[208:211], v158, s[8:9] sc0 sc1
	s_add_u32 s8, s8, 0x2000
	s_addc_u32 s9, s9, 0
	global_load_dwordx4 v[212:215], v158, s[8:9] sc0 sc1
	s_add_u32 s8, s8, 0x2000
	s_addc_u32 s9, s9, 0
	global_load_dwordx4 v[46:49], v158, s[8:9] sc0 sc1
	s_add_u32 s8, s8, 0x2000
	s_addc_u32 s9, s9, 0
	global_load_dwordx4 v[54:57], v158, s[8:9] sc0 sc1
	s_add_u32 s8, s8, 0x2000
	s_addc_u32 s9, s9, 0
	global_load_dwordx4 v[138:141], v158, s[8:9] sc0 sc1
	s_add_u32 s8, s8, 0x2000
	s_addc_u32 s9, s9, 0
	s_waitcnt vmcnt(7)
; __device__ __forceinline__ unsigned pk2(float lo, float hi) { const f32x2 f = {lo, hi}; const bf16n2 v = __builtin_convertvector(f, bf16n2); return __builtin_bit_cast(unsigned, v); }
; __device__ __forceinline__ float sigmoidf_(float x) { return __builtin_amdgcn_rcpf(1.0f + __expf(-x)); }
;     __device__ __forceinline__ bool operator()(f32x4 (&acc)[2][2][4][2], const Unit& u, int wr, int wc, int fr, int fq) const {
;         const int kv = u.pm >> 3; const int row0 = (u.pm & 7) * BM + wr * 64 + fr; const int col0 = wc * 32 + 8 * fq;
;         float bv[2][8];
; #pragma unroll
;         for (int bj = 0; bj < 2; ++bj)
; #pragma unroll
;             for (int j = 0; j < 8; ++j) bv[bj][j] = bh[kv * 256 + col0 + bj * HALF + j];
; #pragma unroll
;         for (int ai = 0; ai < 2; ++ai)
; #pragma unroll
;             for (int m = 0; m < 4; ++m) { bf16_t* rowp = hid + ((size_t)kv * 2048 + row0 + ai * HALF + m * 16) * 256 + col0;
; #pragma unroll
;                 for (int bj = 0; bj < 2; ++bj) { float o[8];
; #pragma unroll
;                     for (int j = 0; j < 8; ++j) { const float x = acc[ai][bj][m][j >> 2][j & 3] + bv[bj][j];
;                         o[j] = x * sigmoidf_(1.5957691216f * (x + 0.044715f * x * x * x)); }
;                     u32x4 w; w.x = pk2(o[0], o[1]); w.y = pk2(o[2], o[3]); w.z = pk2(o[4], o[5]); w.w = pk2(o[6], o[7]);
;                     *(u32x4*)(rowp + bj * HALF) = w; } }
	v_pk_add_f32 v[106:107], v[106:107], v[196:197]
	v_pk_add_f32 v[108:109], v[108:109], v[198:199]
	s_waitcnt vmcnt(6)
	v_pk_add_f32 v[110:111], v[110:111], v[200:201]
	v_pk_add_f32 v[112:113], v[112:113], v[202:203]
	s_waitcnt vmcnt(5)
	v_pk_add_f32 v[114:115], v[114:115], v[204:205]
	v_pk_add_f32 v[116:117], v[116:117], v[206:207]
	s_waitcnt vmcnt(4)
	v_pk_add_f32 v[118:119], v[118:119], v[208:209]
	v_pk_add_f32 v[120:121], v[120:121], v[210:211]
	s_waitcnt vmcnt(3)
	v_pk_add_f32 v[122:123], v[122:123], v[212:213]
	v_pk_add_f32 v[124:125], v[124:125], v[214:215]
	s_waitcnt vmcnt(2)
	v_pk_add_f32 v[126:127], v[126:127], v[46:47]
	v_pk_add_f32 v[128:129], v[128:129], v[48:49]
	s_waitcnt vmcnt(1)
	v_pk_add_f32 v[130:131], v[130:131], v[54:55]
	v_pk_add_f32 v[132:133], v[132:133], v[56:57]
	s_waitcnt vmcnt(0)
	v_pk_add_f32 v[134:135], v[134:135], v[138:139]
	v_pk_add_f32 v[136:137], v[136:137], v[140:141]
	s_ashr_i32 s6, s22, 3
	s_lshl_b32 s7, s22, 8
	v_lshl_or_b32 v46, s6, 8, v150
	v_readlane_b32 s8, v252, 10
	s_and_b32 s7, s7, 0x700
	v_ashrrev_i32_e32 v47, 31, v46
	v_readlane_b32 s9, v252, 11
	v_lshlrev_b32_e32 v0, 1, v150
	s_mov_b32 s22, s37
	v_lshl_add_u64 v[162:163], v[46:47], 2, s[8:9]
	v_add_u32_e32 v46, s7, v164
	s_ashr_i32 s7, s6, 31
	v_ashrrev_i32_e32 v47, 31, v46
	s_lshl_b64 s[6:7], s[6:7], 20
	v_lshlrev_b64 v[46:47], 9, v[46:47]
	v_lshl_add_u64 v[160:161], v[46:47], 0, s[6:7]
	v_lshl_add_u64 v[46:47], s[78:79], 0, v[160:161]
	v_lshl_add_u64 v[158:159], v[46:47], 0, v[0:1]
	global_load_dwordx4 v[46:49], v[162:163], off offset:16
	global_load_dwordx4 v[54:57], v[162:163], off
	s_mov_b64 s[6:7], 0x10000
	s_mov_b64 s[8:9], s[2:3]
	s_waitcnt vmcnt(0)
	v_pk_add_f32 v[38:39], v[38:39], v[46:47]
	v_pk_add_f32 v[66:67], v[66:67], v[54:55]
	v_pk_add_f32 v[68:69], v[68:69], v[56:57]
	v_mul_f32_e32 v0, 0x3d372713, v66
	v_mul_f32_e32 v0, v66, v0
	v_fma_f32 v0, v66, v0, v66
	v_mul_f32_e32 v0, 0x3fcc422a, v0
	v_mul_f32_e32 v0, 0xbfb8aa3b, v0
	v_exp_f32_e32 v0, v0
	v_pk_add_f32 v[40:41], v[40:41], v[48:49]
	v_pk_add_f32 v[126:127], v[126:127], v[54:55]
	v_pk_add_f32 v[128:129], v[128:129], v[56:57]
	v_add_f32_e32 v0, 1.0, v0
	v_rcp_f32_e32 v138, v0
	v_mul_f32_e32 v0, 0x3d372713, v67
	v_mul_f32_e32 v0, v67, v0
	v_fma_f32 v0, v67, v0, v67
	v_mul_f32_e32 v0, 0x3fcc422a, v0
	v_mul_f32_e32 v0, 0xbfb8aa3b, v0
	v_exp_f32_e32 v0, v0
	v_pk_add_f32 v[122:123], v[122:123], v[46:47]
	v_pk_add_f32 v[110:111], v[110:111], v[54:55]
	v_pk_add_f32 v[112:113], v[112:113], v[56:57]
	v_add_f32_e32 v0, 1.0, v0
	v_rcp_f32_e32 v139, v0
	v_mul_f32_e32 v0, 0x3d372713, v68
	v_mul_f32_e32 v0, v68, v0
	v_fma_f32 v0, v68, v0, v68
	v_mul_f32_e32 v0, 0x3fcc422a, v0
	v_mul_f32_e32 v0, 0xbfb8aa3b, v0
	v_exp_f32_e32 v0, v0
	v_pk_mul_f32 v[66:67], v[66:67], v[138:139]
	v_pk_add_f32 v[106:107], v[106:107], v[46:47]
	v_pk_add_f32 v[94:95], v[94:95], v[54:55]
	v_add_f32_e32 v0, 1.0, v0
	v_rcp_f32_e32 v138, v0
	v_mul_f32_e32 v0, 0x3d372713, v69
	v_mul_f32_e32 v0, v69, v0
	v_fma_f32 v0, v69, v0, v69
	v_mul_f32_e32 v0, 0x3fcc422a, v0
	v_mul_f32_e32 v0, 0xbfb8aa3b, v0
	v_exp_f32_e32 v0, v0
	v_pk_add_f32 v[96:97], v[96:97], v[56:57]
	v_pk_add_f32 v[90:91], v[90:91], v[46:47]
	v_pk_add_f32 v[78:79], v[78:79], v[54:55]
	v_add_f32_e32 v0, 1.0, v0
	v_rcp_f32_e32 v139, v0
	v_mul_f32_e32 v0, 0x3d372713, v38
	v_mul_f32_e32 v0, v38, v0
	v_fma_f32 v0, v38, v0, v38
	v_mul_f32_e32 v0, 0x3fcc422a, v0
	v_mul_f32_e32 v0, 0xbfb8aa3b, v0
	v_exp_f32_e32 v0, v0
	v_pk_mul_f32 v[68:69], v[68:69], v[138:139]
	v_pk_add_f32 v[80:81], v[80:81], v[56:57]
	v_pk_add_f32 v[74:75], v[74:75], v[46:47]
	v_add_f32_e32 v0, 1.0, v0
	v_rcp_f32_e32 v138, v0
	v_mul_f32_e32 v0, 0x3d372713, v39
	v_mul_f32_e32 v0, v39, v0
	v_fma_f32 v0, v39, v0, v39
	v_mul_f32_e32 v0, 0x3fcc422a, v0
	v_mul_f32_e32 v0, 0xbfb8aa3b, v0
	v_exp_f32_e32 v0, v0
	v_pk_add_f32 v[58:59], v[58:59], v[54:55]
	v_pk_add_f32 v[60:61], v[60:61], v[56:57]
	v_pk_add_f32 v[50:51], v[50:51], v[46:47]
	v_add_f32_e32 v0, 1.0, v0
	v_rcp_f32_e32 v139, v0
	v_mul_f32_e32 v0, 0x3d372713, v40
	v_mul_f32_e32 v0, v40, v0
	v_fma_f32 v0, v40, v0, v40
	v_mul_f32_e32 v0, 0x3fcc422a, v0
	v_mul_f32_e32 v0, 0xbfb8aa3b, v0
	v_exp_f32_e32 v0, v0
	v_pk_mul_f32 v[38:39], v[38:39], v[138:139]
	v_pk_add_f32 v[30:31], v[30:31], v[54:55]
	v_cvt_pk_bf16_f32 v140, v38, v39
	v_add_f32_e32 v0, 1.0, v0
	v_rcp_f32_e32 v138, v0
	v_mul_f32_e32 v0, 0x3d372713, v41
	v_mul_f32_e32 v0, v41, v0
	v_fma_f32 v0, v41, v0, v41
	v_mul_f32_e32 v0, 0x3fcc422a, v0
	v_mul_f32_e32 v0, 0xbfb8aa3b, v0
	v_exp_f32_e32 v0, v0
	v_pk_add_f32 v[32:33], v[32:33], v[56:57]
	v_pk_add_f32 v[26:27], v[26:27], v[46:47]
	v_pk_add_f32 v[14:15], v[14:15], v[54:55]
	v_add_f32_e32 v0, 1.0, v0
	v_rcp_f32_e32 v139, v0
	v_pk_add_f32 v[16:17], v[16:17], v[56:57]
	v_pk_add_f32 v[10:11], v[10:11], v[46:47]
	v_pk_mul_f32 v[40:41], v[40:41], v[138:139]
	v_cvt_pk_bf16_f32 v138, v66, v67
	v_cvt_pk_bf16_f32 v139, v68, v69
	v_cvt_pk_bf16_f32 v141, v40, v41
	global_load_dwordx4 v[38:41], v[162:163], off offset:528
	global_load_dwordx4 v[66:69], v[162:163], off offset:512
	s_waitcnt vmcnt(0)
; __device__ __forceinline__ unsigned pk2(float lo, float hi) { const f32x2 f = {lo, hi}; const bf16n2 v = __builtin_convertvector(f, bf16n2); return __builtin_bit_cast(unsigned, v); }
; __device__ __forceinline__ float sigmoidf_(float x) { return __builtin_amdgcn_rcpf(1.0f + __expf(-x)); }
;     __device__ __forceinline__ bool operator()(f32x4 (&acc)[2][2][4][2], const Unit& u, int wr, int wc, int fr, int fq) const {
;     ...
;         for (int ai = 0; ai < 2; ++ai)
; #pragma unroll
;             for (int m = 0; m < 4; ++m) { bf16_t* rowp = hid + ((size_t)kv * 2048 + row0 + ai * HALF + m * 16) * 256 + col0;
; #pragma unroll
;                 for (int bj = 0; bj < 2; ++bj) { float o[8];
; #pragma unroll
;                     for (int j = 0; j < 8; ++j) { const float x = acc[ai][bj][m][j >> 2][j & 3] + bv[bj][j];
;                         o[j] = x * sigmoidf_(1.5957691216f * (x + 0.044715f * x * x * x)); }
;                     u32x4 w; w.x = pk2(o[0], o[1]); w.y = pk2(o[2], o[3]); w.z = pk2(o[4], o[5]); w.w = pk2(o[6], o[7]);
;                     *(u32x4*)(rowp + bj * HALF) = w; } }
	v_pk_add_f32 v[130:131], v[130:131], v[38:39]
	v_pk_add_f32 v[134:135], v[134:135], v[66:67]
	v_pk_add_f32 v[136:137], v[136:137], v[68:69]
	v_mul_f32_e32 v0, 0x3d372713, v134
	v_mul_f32_e32 v0, v134, v0
	v_fma_f32 v0, v134, v0, v134
	v_mul_f32_e32 v0, 0x3fcc422a, v0
	v_mul_f32_e32 v0, 0xbfb8aa3b, v0
	v_exp_f32_e32 v0, v0
	global_store_dwordx4 v[158:159], v[138:141], off
	v_pk_add_f32 v[118:119], v[118:119], v[66:67]
	v_pk_add_f32 v[120:121], v[120:121], v[68:69]
	v_add_f32_e32 v0, 1.0, v0
	v_rcp_f32_e32 v162, v0
	v_mul_f32_e32 v0, 0x3d372713, v135
	v_mul_f32_e32 v0, v135, v0
	v_fma_f32 v0, v135, v0, v135
	v_mul_f32_e32 v0, 0x3fcc422a, v0
	v_mul_f32_e32 v0, 0xbfb8aa3b, v0
	v_exp_f32_e32 v0, v0
	v_pk_add_f32 v[114:115], v[114:115], v[38:39]
	v_pk_add_f32 v[102:103], v[102:103], v[66:67]
	v_pk_add_f32 v[104:105], v[104:105], v[68:69]
	v_add_f32_e32 v0, 1.0, v0
	v_rcp_f32_e32 v163, v0
	v_mul_f32_e32 v0, 0x3d372713, v136
	v_mul_f32_e32 v0, v136, v0
	v_fma_f32 v0, v136, v0, v136
	v_mul_f32_e32 v0, 0x3fcc422a, v0
	v_mul_f32_e32 v0, 0xbfb8aa3b, v0
	v_exp_f32_e32 v0, v0
	v_pk_mul_f32 v[134:135], v[134:135], v[162:163]
	v_pk_add_f32 v[98:99], v[98:99], v[38:39]
	v_pk_add_f32 v[86:87], v[86:87], v[66:67]
	v_add_f32_e32 v0, 1.0, v0
	v_rcp_f32_e32 v162, v0
	v_mul_f32_e32 v0, 0x3d372713, v137
	v_mul_f32_e32 v0, v137, v0
	v_fma_f32 v0, v137, v0, v137
	v_mul_f32_e32 v0, 0x3fcc422a, v0
	v_mul_f32_e32 v0, 0xbfb8aa3b, v0
	v_exp_f32_e32 v0, v0
	v_pk_add_f32 v[88:89], v[88:89], v[68:69]
	v_pk_add_f32 v[82:83], v[82:83], v[38:39]
	v_pk_add_f32 v[70:71], v[70:71], v[66:67]
	v_add_f32_e32 v0, 1.0, v0
	v_rcp_f32_e32 v163, v0
	v_mul_f32_e32 v0, 0x3d372713, v130
	v_mul_f32_e32 v0, v130, v0
	v_fma_f32 v0, v130, v0, v130
	v_mul_f32_e32 v0, 0x3fcc422a, v0
	v_mul_f32_e32 v0, 0xbfb8aa3b, v0
	v_exp_f32_e32 v0, v0
	v_pk_mul_f32 v[136:137], v[136:137], v[162:163]
	v_pk_add_f32 v[72:73], v[72:73], v[68:69]
	v_pk_add_f32 v[62:63], v[62:63], v[38:39]
	v_add_f32_e32 v0, 1.0, v0
	v_rcp_f32_e32 v162, v0
	v_mul_f32_e32 v0, 0x3d372713, v131
	v_mul_f32_e32 v0, v131, v0
	v_fma_f32 v0, v131, v0, v131
	v_mul_f32_e32 v0, 0x3fcc422a, v0
	v_mul_f32_e32 v0, 0xbfb8aa3b, v0
	v_exp_f32_e32 v0, v0
	v_pk_add_f32 v[42:43], v[42:43], v[66:67]
	v_pk_add_f32 v[44:45], v[44:45], v[68:69]
	v_pk_add_f32 v[34:35], v[34:35], v[38:39]
	v_add_f32_e32 v0, 1.0, v0
	v_rcp_f32_e32 v163, v0
	v_pk_add_f32 v[22:23], v[22:23], v[66:67]
	v_pk_add_f32 v[24:25], v[24:25], v[68:69]
	v_pk_add_f32 v[18:19], v[18:19], v[38:39]
	v_pk_mul_f32 v[162:163], v[130:131], v[162:163]
	v_pk_add_f32 v[130:131], v[132:133], v[40:41]
	v_pk_add_f32 v[6:7], v[6:7], v[66:67]
	v_mul_f32_e32 v0, 0x3d372713, v130
	v_mul_f32_e32 v0, v130, v0
	v_fma_f32 v0, v130, v0, v130
	v_mul_f32_e32 v0, 0x3fcc422a, v0
	v_mul_f32_e32 v0, 0xbfb8aa3b, v0
	v_exp_f32_e32 v0, v0
	v_pk_add_f32 v[8:9], v[8:9], v[68:69]
	v_pk_add_f32 v[2:3], v[2:3], v[38:39]
	v_add_f32_e32 v0, 1.0, v0
	v_rcp_f32_e32 v132, v0
	v_mul_f32_e32 v0, 0x3d372713, v131
	v_mul_f32_e32 v0, v131, v0
	v_fma_f32 v0, v131, v0, v131
	v_mul_f32_e32 v0, 0x3fcc422a, v0
	v_mul_f32_e32 v0, 0xbfb8aa3b, v0
	v_exp_f32_e32 v0, v0
	s_nop 0
	v_add_f32_e32 v0, 1.0, v0
	v_rcp_f32_e32 v133, v0
	v_mul_f32_e32 v0, 0x3d372713, v126
	v_mul_f32_e32 v0, v126, v0
	v_fma_f32 v0, v126, v0, v126
	v_mul_f32_e32 v0, 0x3fcc422a, v0
	v_mul_f32_e32 v0, 0xbfb8aa3b, v0
	v_exp_f32_e32 v0, v0
	v_pk_mul_f32 v[138:139], v[130:131], v[132:133]
	v_cvt_pk_bf16_f32 v130, v134, v135
	v_cvt_pk_bf16_f32 v131, v136, v137
	v_cvt_pk_bf16_f32 v132, v162, v163
	v_cvt_pk_bf16_f32 v133, v138, v139
	v_add_f32_e32 v0, 1.0, v0
	global_store_dwordx4 v[158:159], v[130:133], off offset:256
	s_nop 1
	v_rcp_f32_e32 v132, v0
	v_mul_f32_e32 v0, 0x3d372713, v127
	v_mul_f32_e32 v0, v127, v0
	v_fma_f32 v0, v127, v0, v127
	v_mul_f32_e32 v0, 0x3fcc422a, v0
	v_mul_f32_e32 v0, 0xbfb8aa3b, v0
	v_exp_f32_e32 v0, v0
	v_or_b32_e32 v130, 0x2000, v160
	v_mov_b32_e32 v131, v161
	v_lshl_add_u64 v[130:131], v[152:153], 0, v[130:131]
	v_add_f32_e32 v0, 1.0, v0
	v_rcp_f32_e32 v133, v0
	v_mul_f32_e32 v0, 0x3d372713, v128
	v_mul_f32_e32 v0, v128, v0
	v_fma_f32 v0, v128, v0, v128
	v_mul_f32_e32 v0, 0x3fcc422a, v0
	v_mul_f32_e32 v0, 0xbfb8aa3b, v0
	v_exp_f32_e32 v0, v0
	v_pk_mul_f32 v[126:127], v[126:127], v[132:133]
	v_add_f32_e32 v0, 1.0, v0
	v_rcp_f32_e32 v132, v0
	v_mul_f32_e32 v0, 0x3d372713, v129
	v_mul_f32_e32 v0, v129, v0
	v_fma_f32 v0, v129, v0, v129
	v_mul_f32_e32 v0, 0x3fcc422a, v0
	v_mul_f32_e32 v0, 0xbfb8aa3b, v0
	v_exp_f32_e32 v0, v0
	s_nop 0
	v_add_f32_e32 v0, 1.0, v0
	v_rcp_f32_e32 v133, v0
	v_mul_f32_e32 v0, 0x3d372713, v122
	v_mul_f32_e32 v0, v122, v0
	v_fma_f32 v0, v122, v0, v122
	v_mul_f32_e32 v0, 0x3fcc422a, v0
	v_mul_f32_e32 v0, 0xbfb8aa3b, v0
	v_exp_f32_e32 v0, v0
	v_pk_mul_f32 v[128:129], v[128:129], v[132:133]
	v_add_f32_e32 v0, 1.0, v0
	v_rcp_f32_e32 v132, v0
	v_mul_f32_e32 v0, 0x3d372713, v123
	v_mul_f32_e32 v0, v123, v0
	v_fma_f32 v0, v123, v0, v123
	v_mul_f32_e32 v0, 0x3fcc422a, v0
	v_mul_f32_e32 v0, 0xbfb8aa3b, v0
	v_exp_f32_e32 v0, v0
	s_nop 0
	v_add_f32_e32 v0, 1.0, v0
	v_rcp_f32_e32 v133, v0
	s_nop 0
	v_pk_mul_f32 v[132:133], v[122:123], v[132:133]
	v_pk_add_f32 v[122:123], v[124:125], v[48:49]
	s_nop 0
	v_mul_f32_e32 v0, 0x3d372713, v122
	v_mul_f32_e32 v0, v122, v0
	v_fma_f32 v0, v122, v0, v122
	v_mul_f32_e32 v0, 0x3fcc422a, v0
	v_mul_f32_e32 v0, 0xbfb8aa3b, v0
	v_exp_f32_e32 v0, v0
	s_nop 0
	v_add_f32_e32 v0, 1.0, v0
	v_rcp_f32_e32 v124, v0
	v_mul_f32_e32 v0, 0x3d372713, v123
	v_mul_f32_e32 v0, v123, v0
	v_fma_f32 v0, v123, v0, v123
	v_mul_f32_e32 v0, 0x3fcc422a, v0
	v_mul_f32_e32 v0, 0xbfb8aa3b, v0
	v_exp_f32_e32 v0, v0
	s_nop 0
; __device__ __forceinline__ unsigned pk2(float lo, float hi) { const f32x2 f = {lo, hi}; const bf16n2 v = __builtin_convertvector(f, bf16n2); return __builtin_bit_cast(unsigned, v); }
; __device__ __forceinline__ float sigmoidf_(float x) { return __builtin_amdgcn_rcpf(1.0f + __expf(-x)); }
;     __device__ __forceinline__ bool operator()(f32x4 (&acc)[2][2][4][2], const Unit& u, int wr, int wc, int fr, int fq) const {
;     ...
;         for (int ai = 0; ai < 2; ++ai)
; #pragma unroll
;             for (int m = 0; m < 4; ++m) { bf16_t* rowp = hid + ((size_t)kv * 2048 + row0 + ai * HALF + m * 16) * 256 + col0;
; #pragma unroll
;                 for (int bj = 0; bj < 2; ++bj) { float o[8];
; #pragma unroll
;                     for (int j = 0; j < 8; ++j) { const float x = acc[ai][bj][m][j >> 2][j & 3] + bv[bj][j];
;                         o[j] = x * sigmoidf_(1.5957691216f * (x + 0.044715f * x * x * x)); }
;                     u32x4 w; w.x = pk2(o[0], o[1]); w.y = pk2(o[2], o[3]); w.z = pk2(o[4], o[5]); w.w = pk2(o[6], o[7]);
;                     *(u32x4*)(rowp + bj * HALF) = w; } }
	v_add_f32_e32 v0, 1.0, v0
	v_rcp_f32_e32 v125, v0
	v_mul_f32_e32 v0, 0x3d372713, v118
	v_mul_f32_e32 v0, v118, v0
	v_fma_f32 v0, v118, v0, v118
	v_mul_f32_e32 v0, 0x3fcc422a, v0
	v_mul_f32_e32 v0, 0xbfb8aa3b, v0
	v_exp_f32_e32 v0, v0
	v_pk_mul_f32 v[134:135], v[122:123], v[124:125]
	v_cvt_pk_bf16_f32 v122, v126, v127
	v_cvt_pk_bf16_f32 v123, v128, v129
	v_cvt_pk_bf16_f32 v124, v132, v133
	v_cvt_pk_bf16_f32 v125, v134, v135
	v_add_f32_e32 v0, 1.0, v0
	global_store_dwordx4 v[130:131], v[122:125], off
	s_nop 1
	v_rcp_f32_e32 v122, v0
	v_mul_f32_e32 v0, 0x3d372713, v119
	v_mul_f32_e32 v0, v119, v0
	v_fma_f32 v0, v119, v0, v119
	v_mul_f32_e32 v0, 0x3fcc422a, v0
	v_mul_f32_e32 v0, 0xbfb8aa3b, v0
	v_exp_f32_e32 v0, v0
	s_nop 0
	v_add_f32_e32 v0, 1.0, v0
	v_rcp_f32_e32 v123, v0
	v_mul_f32_e32 v0, 0x3d372713, v120
	v_mul_f32_e32 v0, v120, v0
	v_fma_f32 v0, v120, v0, v120
	v_mul_f32_e32 v0, 0x3fcc422a, v0
	v_mul_f32_e32 v0, 0xbfb8aa3b, v0
	v_exp_f32_e32 v0, v0
	v_pk_mul_f32 v[118:119], v[118:119], v[122:123]
	v_add_f32_e32 v0, 1.0, v0
	v_rcp_f32_e32 v122, v0
	v_mul_f32_e32 v0, 0x3d372713, v121
	v_mul_f32_e32 v0, v121, v0
	v_fma_f32 v0, v121, v0, v121
	v_mul_f32_e32 v0, 0x3fcc422a, v0
	v_mul_f32_e32 v0, 0xbfb8aa3b, v0
	v_exp_f32_e32 v0, v0
	s_nop 0
	v_add_f32_e32 v0, 1.0, v0
	v_rcp_f32_e32 v123, v0
	v_mul_f32_e32 v0, 0x3d372713, v114
	v_mul_f32_e32 v0, v114, v0
	v_fma_f32 v0, v114, v0, v114
	v_mul_f32_e32 v0, 0x3fcc422a, v0
	v_mul_f32_e32 v0, 0xbfb8aa3b, v0
	v_exp_f32_e32 v0, v0
	v_pk_mul_f32 v[120:121], v[120:121], v[122:123]
	v_add_f32_e32 v0, 1.0, v0
	v_rcp_f32_e32 v122, v0
	v_mul_f32_e32 v0, 0x3d372713, v115
	v_mul_f32_e32 v0, v115, v0
	v_fma_f32 v0, v115, v0, v115
	v_mul_f32_e32 v0, 0x3fcc422a, v0
	v_mul_f32_e32 v0, 0xbfb8aa3b, v0
	v_exp_f32_e32 v0, v0
	s_nop 0
	v_add_f32_e32 v0, 1.0, v0
	v_rcp_f32_e32 v123, v0
	s_nop 0
	v_pk_mul_f32 v[122:123], v[114:115], v[122:123]
	v_pk_add_f32 v[114:115], v[116:117], v[40:41]
	s_nop 0
	v_mul_f32_e32 v0, 0x3d372713, v114
	v_mul_f32_e32 v0, v114, v0
	v_fma_f32 v0, v114, v0, v114
	v_mul_f32_e32 v0, 0x3fcc422a, v0
	v_mul_f32_e32 v0, 0xbfb8aa3b, v0
	v_exp_f32_e32 v0, v0
	s_nop 0
	v_add_f32_e32 v0, 1.0, v0
	v_rcp_f32_e32 v116, v0
	v_mul_f32_e32 v0, 0x3d372713, v115
	v_mul_f32_e32 v0, v115, v0
	v_fma_f32 v0, v115, v0, v115
	v_mul_f32_e32 v0, 0x3fcc422a, v0
	v_mul_f32_e32 v0, 0xbfb8aa3b, v0
	v_exp_f32_e32 v0, v0
	s_nop 0
	v_add_f32_e32 v0, 1.0, v0
	v_rcp_f32_e32 v117, v0
	v_mul_f32_e32 v0, 0x3d372713, v110
	v_mul_f32_e32 v0, v110, v0
	v_fma_f32 v0, v110, v0, v110
	v_mul_f32_e32 v0, 0x3fcc422a, v0
	v_mul_f32_e32 v0, 0xbfb8aa3b, v0
	v_exp_f32_e32 v0, v0
	v_pk_mul_f32 v[124:125], v[114:115], v[116:117]
	v_cvt_pk_bf16_f32 v114, v118, v119
	v_cvt_pk_bf16_f32 v115, v120, v121
	v_cvt_pk_bf16_f32 v116, v122, v123
	v_cvt_pk_bf16_f32 v117, v124, v125
	v_add_f32_e32 v0, 1.0, v0
	global_store_dwordx4 v[130:131], v[114:117], off offset:256
	s_nop 1
	v_rcp_f32_e32 v116, v0
	v_mul_f32_e32 v0, 0x3d372713, v111
	v_mul_f32_e32 v0, v111, v0
	v_fma_f32 v0, v111, v0, v111
	v_mul_f32_e32 v0, 0x3fcc422a, v0
	v_mul_f32_e32 v0, 0xbfb8aa3b, v0
	v_exp_f32_e32 v0, v0
	v_or_b32_e32 v114, 0x4000, v160
	v_mov_b32_e32 v115, v161
	v_lshl_add_u64 v[114:115], v[152:153], 0, v[114:115]
	v_add_f32_e32 v0, 1.0, v0
	v_rcp_f32_e32 v117, v0
	v_mul_f32_e32 v0, 0x3d372713, v112
	v_mul_f32_e32 v0, v112, v0
	v_fma_f32 v0, v112, v0, v112
	v_mul_f32_e32 v0, 0x3fcc422a, v0
	v_mul_f32_e32 v0, 0xbfb8aa3b, v0
	v_exp_f32_e32 v0, v0
	v_pk_mul_f32 v[110:111], v[110:111], v[116:117]
	v_or_b32_e32 v160, 0x6000, v160
	v_add_f32_e32 v0, 1.0, v0
	v_rcp_f32_e32 v116, v0
	v_mul_f32_e32 v0, 0x3d372713, v113
	v_mul_f32_e32 v0, v113, v0
	v_fma_f32 v0, v113, v0, v113
	v_mul_f32_e32 v0, 0x3fcc422a, v0
	v_mul_f32_e32 v0, 0xbfb8aa3b, v0
	v_exp_f32_e32 v0, v0
	s_nop 0
	v_add_f32_e32 v0, 1.0, v0
	v_rcp_f32_e32 v117, v0
	v_mul_f32_e32 v0, 0x3d372713, v106
	v_mul_f32_e32 v0, v106, v0
	v_fma_f32 v0, v106, v0, v106
	v_mul_f32_e32 v0, 0x3fcc422a, v0
	v_mul_f32_e32 v0, 0xbfb8aa3b, v0
	v_exp_f32_e32 v0, v0
	v_pk_mul_f32 v[112:113], v[112:113], v[116:117]
	v_add_f32_e32 v0, 1.0, v0
	v_rcp_f32_e32 v116, v0
	v_mul_f32_e32 v0, 0x3d372713, v107
	v_mul_f32_e32 v0, v107, v0
	v_fma_f32 v0, v107, v0, v107
	v_mul_f32_e32 v0, 0x3fcc422a, v0
	v_mul_f32_e32 v0, 0xbfb8aa3b, v0
	v_exp_f32_e32 v0, v0
	s_nop 0
	v_add_f32_e32 v0, 1.0, v0
	v_rcp_f32_e32 v117, v0
	s_nop 0
	v_pk_mul_f32 v[116:117], v[106:107], v[116:117]
	v_pk_add_f32 v[106:107], v[108:109], v[48:49]
	s_nop 0
	v_mul_f32_e32 v0, 0x3d372713, v106
	v_mul_f32_e32 v0, v106, v0
	v_fma_f32 v0, v106, v0, v106
	v_mul_f32_e32 v0, 0x3fcc422a, v0
	v_mul_f32_e32 v0, 0xbfb8aa3b, v0
	v_exp_f32_e32 v0, v0
	s_nop 0
	v_add_f32_e32 v0, 1.0, v0
	v_rcp_f32_e32 v108, v0
	v_mul_f32_e32 v0, 0x3d372713, v107
	v_mul_f32_e32 v0, v107, v0
	v_fma_f32 v0, v107, v0, v107
	v_mul_f32_e32 v0, 0x3fcc422a, v0
	v_mul_f32_e32 v0, 0xbfb8aa3b, v0
	v_exp_f32_e32 v0, v0
	s_nop 0
	v_add_f32_e32 v0, 1.0, v0
	v_rcp_f32_e32 v109, v0
	v_mul_f32_e32 v0, 0x3d372713, v102
	v_mul_f32_e32 v0, v102, v0
	v_fma_f32 v0, v102, v0, v102
	v_mul_f32_e32 v0, 0x3fcc422a, v0
	v_mul_f32_e32 v0, 0xbfb8aa3b, v0
	v_exp_f32_e32 v0, v0
	v_pk_mul_f32 v[118:119], v[106:107], v[108:109]
	v_cvt_pk_bf16_f32 v106, v110, v111
	v_cvt_pk_bf16_f32 v107, v112, v113
	v_cvt_pk_bf16_f32 v108, v116, v117
	v_cvt_pk_bf16_f32 v109, v118, v119
	v_add_f32_e32 v0, 1.0, v0
	global_store_dwordx4 v[114:115], v[106:109], off
	s_nop 1
	v_rcp_f32_e32 v106, v0
	v_mul_f32_e32 v0, 0x3d372713, v103
	v_mul_f32_e32 v0, v103, v0
	v_fma_f32 v0, v103, v0, v103
	v_mul_f32_e32 v0, 0x3fcc422a, v0
	v_mul_f32_e32 v0, 0xbfb8aa3b, v0
	v_exp_f32_e32 v0, v0
; __device__ __forceinline__ unsigned pk2(float lo, float hi) { const f32x2 f = {lo, hi}; const bf16n2 v = __builtin_convertvector(f, bf16n2); return __builtin_bit_cast(unsigned, v); }
; __device__ __forceinline__ float sigmoidf_(float x) { return __builtin_amdgcn_rcpf(1.0f + __expf(-x)); }
;     __device__ __forceinline__ bool operator()(f32x4 (&acc)[2][2][4][2], const Unit& u, int wr, int wc, int fr, int fq) const {
;     ...
;         for (int ai = 0; ai < 2; ++ai)
; #pragma unroll
;             for (int m = 0; m < 4; ++m) { bf16_t* rowp = hid + ((size_t)kv * 2048 + row0 + ai * HALF + m * 16) * 256 + col0;
; #pragma unroll
;                 for (int bj = 0; bj < 2; ++bj) { float o[8];
; #pragma unroll
;                     for (int j = 0; j < 8; ++j) { const float x = acc[ai][bj][m][j >> 2][j & 3] + bv[bj][j];
;                         o[j] = x * sigmoidf_(1.5957691216f * (x + 0.044715f * x * x * x)); }
;                     u32x4 w; w.x = pk2(o[0], o[1]); w.y = pk2(o[2], o[3]); w.z = pk2(o[4], o[5]); w.w = pk2(o[6], o[7]);
;                     *(u32x4*)(rowp + bj * HALF) = w; } }
	s_nop 0
	v_add_f32_e32 v0, 1.0, v0
	v_rcp_f32_e32 v107, v0
	v_mul_f32_e32 v0, 0x3d372713, v104
	v_mul_f32_e32 v0, v104, v0
	v_fma_f32 v0, v104, v0, v104
	v_mul_f32_e32 v0, 0x3fcc422a, v0
	v_mul_f32_e32 v0, 0xbfb8aa3b, v0
	v_exp_f32_e32 v0, v0
	v_pk_mul_f32 v[102:103], v[102:103], v[106:107]
	v_add_f32_e32 v0, 1.0, v0
	v_rcp_f32_e32 v106, v0
	v_mul_f32_e32 v0, 0x3d372713, v105
	v_mul_f32_e32 v0, v105, v0
	v_fma_f32 v0, v105, v0, v105
	v_mul_f32_e32 v0, 0x3fcc422a, v0
	v_mul_f32_e32 v0, 0xbfb8aa3b, v0
	v_exp_f32_e32 v0, v0
	s_nop 0
	v_add_f32_e32 v0, 1.0, v0
	v_rcp_f32_e32 v107, v0
	v_mul_f32_e32 v0, 0x3d372713, v98
	v_mul_f32_e32 v0, v98, v0
	v_fma_f32 v0, v98, v0, v98
	v_mul_f32_e32 v0, 0x3fcc422a, v0
	v_mul_f32_e32 v0, 0xbfb8aa3b, v0
	v_exp_f32_e32 v0, v0
	v_pk_mul_f32 v[104:105], v[104:105], v[106:107]
	v_add_f32_e32 v0, 1.0, v0
	v_rcp_f32_e32 v106, v0
	v_mul_f32_e32 v0, 0x3d372713, v99
	v_mul_f32_e32 v0, v99, v0
	v_fma_f32 v0, v99, v0, v99
	v_mul_f32_e32 v0, 0x3fcc422a, v0
	v_mul_f32_e32 v0, 0xbfb8aa3b, v0
	v_exp_f32_e32 v0, v0
	s_nop 0
	v_add_f32_e32 v0, 1.0, v0
	v_rcp_f32_e32 v107, v0
	s_nop 0
	v_pk_mul_f32 v[106:107], v[98:99], v[106:107]
	v_pk_add_f32 v[98:99], v[100:101], v[40:41]
	s_nop 0
	v_mul_f32_e32 v0, 0x3d372713, v98
	v_mul_f32_e32 v0, v98, v0
	v_fma_f32 v0, v98, v0, v98
	v_mul_f32_e32 v0, 0x3fcc422a, v0
	v_mul_f32_e32 v0, 0xbfb8aa3b, v0
	v_exp_f32_e32 v0, v0
	s_nop 0
	v_add_f32_e32 v0, 1.0, v0
	v_rcp_f32_e32 v100, v0
	v_mul_f32_e32 v0, 0x3d372713, v99
	v_mul_f32_e32 v0, v99, v0
	v_fma_f32 v0, v99, v0, v99
	v_mul_f32_e32 v0, 0x3fcc422a, v0
	v_mul_f32_e32 v0, 0xbfb8aa3b, v0
	v_exp_f32_e32 v0, v0
	s_nop 0
	v_add_f32_e32 v0, 1.0, v0
	v_rcp_f32_e32 v101, v0
	v_mul_f32_e32 v0, 0x3d372713, v94
	v_mul_f32_e32 v0, v94, v0
	v_fma_f32 v0, v94, v0, v94
	v_mul_f32_e32 v0, 0x3fcc422a, v0
	v_mul_f32_e32 v0, 0xbfb8aa3b, v0
	v_exp_f32_e32 v0, v0
	v_pk_mul_f32 v[108:109], v[98:99], v[100:101]
	v_cvt_pk_bf16_f32 v98, v102, v103
	v_cvt_pk_bf16_f32 v99, v104, v105
	v_cvt_pk_bf16_f32 v100, v106, v107
	v_cvt_pk_bf16_f32 v101, v108, v109
	v_add_f32_e32 v0, 1.0, v0
	global_store_dwordx4 v[114:115], v[98:101], off offset:256
	s_nop 1
	v_rcp_f32_e32 v100, v0
	v_mul_f32_e32 v0, 0x3d372713, v95
	v_mul_f32_e32 v0, v95, v0
	v_fma_f32 v0, v95, v0, v95
	v_mul_f32_e32 v0, 0x3fcc422a, v0
	v_mul_f32_e32 v0, 0xbfb8aa3b, v0
	v_exp_f32_e32 v0, v0
	v_lshl_add_u64 v[98:99], v[152:153], 0, v[160:161]
	v_add_f32_e32 v0, 1.0, v0
	v_rcp_f32_e32 v101, v0
	v_mul_f32_e32 v0, 0x3d372713, v96
	v_mul_f32_e32 v0, v96, v0
	v_fma_f32 v0, v96, v0, v96
	v_mul_f32_e32 v0, 0x3fcc422a, v0
	v_mul_f32_e32 v0, 0xbfb8aa3b, v0
	v_exp_f32_e32 v0, v0
	v_pk_mul_f32 v[94:95], v[94:95], v[100:101]
	v_add_f32_e32 v0, 1.0, v0
	v_rcp_f32_e32 v100, v0
	v_mul_f32_e32 v0, 0x3d372713, v97
	v_mul_f32_e32 v0, v97, v0
	v_fma_f32 v0, v97, v0, v97
	v_mul_f32_e32 v0, 0x3fcc422a, v0
	v_mul_f32_e32 v0, 0xbfb8aa3b, v0
	v_exp_f32_e32 v0, v0
	s_nop 0
	v_add_f32_e32 v0, 1.0, v0
	v_rcp_f32_e32 v101, v0
	v_mul_f32_e32 v0, 0x3d372713, v90
	v_mul_f32_e32 v0, v90, v0
	v_fma_f32 v0, v90, v0, v90
	v_mul_f32_e32 v0, 0x3fcc422a, v0
	v_mul_f32_e32 v0, 0xbfb8aa3b, v0
	v_exp_f32_e32 v0, v0
	v_pk_mul_f32 v[96:97], v[96:97], v[100:101]
	v_add_f32_e32 v0, 1.0, v0
	v_rcp_f32_e32 v100, v0
	v_mul_f32_e32 v0, 0x3d372713, v91
	v_mul_f32_e32 v0, v91, v0
	v_fma_f32 v0, v91, v0, v91
	v_mul_f32_e32 v0, 0x3fcc422a, v0
	v_mul_f32_e32 v0, 0xbfb8aa3b, v0
	v_exp_f32_e32 v0, v0
	s_nop 0
	v_add_f32_e32 v0, 1.0, v0
	v_rcp_f32_e32 v101, v0
	s_nop 0
	v_pk_mul_f32 v[100:101], v[90:91], v[100:101]
	v_pk_add_f32 v[90:91], v[92:93], v[48:49]
	s_nop 0
	v_mul_f32_e32 v0, 0x3d372713, v90
	v_mul_f32_e32 v0, v90, v0
	v_fma_f32 v0, v90, v0, v90
	v_mul_f32_e32 v0, 0x3fcc422a, v0
	v_mul_f32_e32 v0, 0xbfb8aa3b, v0
	v_exp_f32_e32 v0, v0
	s_nop 0
	v_add_f32_e32 v0, 1.0, v0
	v_rcp_f32_e32 v92, v0
	v_mul_f32_e32 v0, 0x3d372713, v91
	v_mul_f32_e32 v0, v91, v0
	v_fma_f32 v0, v91, v0, v91
	v_mul_f32_e32 v0, 0x3fcc422a, v0
	v_mul_f32_e32 v0, 0xbfb8aa3b, v0
	v_exp_f32_e32 v0, v0
	s_nop 0
	v_add_f32_e32 v0, 1.0, v0
	v_rcp_f32_e32 v93, v0
	v_mul_f32_e32 v0, 0x3d372713, v86
	v_mul_f32_e32 v0, v86, v0
	v_fma_f32 v0, v86, v0, v86
	v_mul_f32_e32 v0, 0x3fcc422a, v0
	v_mul_f32_e32 v0, 0xbfb8aa3b, v0
	v_exp_f32_e32 v0, v0
	v_pk_mul_f32 v[102:103], v[90:91], v[92:93]
	v_cvt_pk_bf16_f32 v90, v94, v95
	v_cvt_pk_bf16_f32 v91, v96, v97
	v_cvt_pk_bf16_f32 v92, v100, v101
	v_cvt_pk_bf16_f32 v93, v102, v103
	v_add_f32_e32 v0, 1.0, v0
	global_store_dwordx4 v[98:99], v[90:93], off
	s_nop 1
	v_rcp_f32_e32 v90, v0
	v_mul_f32_e32 v0, 0x3d372713, v87
	v_mul_f32_e32 v0, v87, v0
	v_fma_f32 v0, v87, v0, v87
	v_mul_f32_e32 v0, 0x3fcc422a, v0
	v_mul_f32_e32 v0, 0xbfb8aa3b, v0
	v_exp_f32_e32 v0, v0
	s_nop 0
	v_add_f32_e32 v0, 1.0, v0
	v_rcp_f32_e32 v91, v0
	v_mul_f32_e32 v0, 0x3d372713, v88
	v_mul_f32_e32 v0, v88, v0
	v_fma_f32 v0, v88, v0, v88
	v_mul_f32_e32 v0, 0x3fcc422a, v0
	v_mul_f32_e32 v0, 0xbfb8aa3b, v0
	v_exp_f32_e32 v0, v0
	v_pk_mul_f32 v[86:87], v[86:87], v[90:91]
	v_add_f32_e32 v0, 1.0, v0
	v_rcp_f32_e32 v90, v0
	v_mul_f32_e32 v0, 0x3d372713, v89
	v_mul_f32_e32 v0, v89, v0
	v_fma_f32 v0, v89, v0, v89
	v_mul_f32_e32 v0, 0x3fcc422a, v0
	v_mul_f32_e32 v0, 0xbfb8aa3b, v0
	v_exp_f32_e32 v0, v0
	s_nop 0
	v_add_f32_e32 v0, 1.0, v0
	v_rcp_f32_e32 v91, v0
	v_mul_f32_e32 v0, 0x3d372713, v82
	v_mul_f32_e32 v0, v82, v0
	v_fma_f32 v0, v82, v0, v82
	v_mul_f32_e32 v0, 0x3fcc422a, v0
	v_mul_f32_e32 v0, 0xbfb8aa3b, v0
	v_exp_f32_e32 v0, v0
	v_pk_mul_f32 v[88:89], v[88:89], v[90:91]
	v_add_f32_e32 v0, 1.0, v0
	v_rcp_f32_e32 v90, v0
	v_mul_f32_e32 v0, 0x3d372713, v83
	v_mul_f32_e32 v0, v83, v0
; __device__ __forceinline__ unsigned pk2(float lo, float hi) { const f32x2 f = {lo, hi}; const bf16n2 v = __builtin_convertvector(f, bf16n2); return __builtin_bit_cast(unsigned, v); }
; __device__ __forceinline__ float sigmoidf_(float x) { return __builtin_amdgcn_rcpf(1.0f + __expf(-x)); }
;     __device__ __forceinline__ bool operator()(f32x4 (&acc)[2][2][4][2], const Unit& u, int wr, int wc, int fr, int fq) const {
;     ...
;         for (int ai = 0; ai < 2; ++ai)
; #pragma unroll
;             for (int m = 0; m < 4; ++m) { bf16_t* rowp = hid + ((size_t)kv * 2048 + row0 + ai * HALF + m * 16) * 256 + col0;
; #pragma unroll
;                 for (int bj = 0; bj < 2; ++bj) { float o[8];
; #pragma unroll
;                     for (int j = 0; j < 8; ++j) { const float x = acc[ai][bj][m][j >> 2][j & 3] + bv[bj][j];
;                         o[j] = x * sigmoidf_(1.5957691216f * (x + 0.044715f * x * x * x)); }
;                     u32x4 w; w.x = pk2(o[0], o[1]); w.y = pk2(o[2], o[3]); w.z = pk2(o[4], o[5]); w.w = pk2(o[6], o[7]);
;                     *(u32x4*)(rowp + bj * HALF) = w; } }
	v_fma_f32 v0, v83, v0, v83
	v_mul_f32_e32 v0, 0x3fcc422a, v0
	v_mul_f32_e32 v0, 0xbfb8aa3b, v0
	v_exp_f32_e32 v0, v0
	s_nop 0
	v_add_f32_e32 v0, 1.0, v0
	v_rcp_f32_e32 v91, v0
	s_nop 0
	v_pk_mul_f32 v[90:91], v[82:83], v[90:91]
	v_pk_add_f32 v[82:83], v[84:85], v[40:41]
	s_nop 0
	v_mul_f32_e32 v0, 0x3d372713, v82
	v_mul_f32_e32 v0, v82, v0
	v_fma_f32 v0, v82, v0, v82
	v_mul_f32_e32 v0, 0x3fcc422a, v0
	v_mul_f32_e32 v0, 0xbfb8aa3b, v0
	v_exp_f32_e32 v0, v0
	s_nop 0
	v_add_f32_e32 v0, 1.0, v0
	v_rcp_f32_e32 v84, v0
	v_mul_f32_e32 v0, 0x3d372713, v83
	v_mul_f32_e32 v0, v83, v0
	v_fma_f32 v0, v83, v0, v83
	v_mul_f32_e32 v0, 0x3fcc422a, v0
	v_mul_f32_e32 v0, 0xbfb8aa3b, v0
	v_exp_f32_e32 v0, v0
	s_nop 0
	v_add_f32_e32 v0, 1.0, v0
	v_rcp_f32_e32 v85, v0
	v_mul_f32_e32 v0, 0x3d372713, v78
	v_mul_f32_e32 v0, v78, v0
	v_fma_f32 v0, v78, v0, v78
	v_mul_f32_e32 v0, 0x3fcc422a, v0
	v_mul_f32_e32 v0, 0xbfb8aa3b, v0
	v_exp_f32_e32 v0, v0
	v_pk_mul_f32 v[92:93], v[82:83], v[84:85]
	v_cvt_pk_bf16_f32 v82, v86, v87
	v_cvt_pk_bf16_f32 v83, v88, v89
	v_cvt_pk_bf16_f32 v84, v90, v91
	v_cvt_pk_bf16_f32 v85, v92, v93
	v_add_f32_e32 v0, 1.0, v0
	global_store_dwordx4 v[98:99], v[82:85], off offset:256
	s_nop 1
	v_rcp_f32_e32 v84, v0
	v_mul_f32_e32 v0, 0x3d372713, v79
	v_mul_f32_e32 v0, v79, v0
	v_fma_f32 v0, v79, v0, v79
	v_mul_f32_e32 v0, 0x3fcc422a, v0
	v_mul_f32_e32 v0, 0xbfb8aa3b, v0
	v_exp_f32_e32 v0, v0
	v_lshl_add_u64 v[82:83], v[158:159], 0, s[6:7]
	s_mov_b32 s6, 0x10000
	v_add_f32_e32 v0, 1.0, v0
	v_rcp_f32_e32 v85, v0
	v_mul_f32_e32 v0, 0x3d372713, v80
	v_mul_f32_e32 v0, v80, v0
	v_fma_f32 v0, v80, v0, v80
	v_mul_f32_e32 v0, 0x3fcc422a, v0
	v_mul_f32_e32 v0, 0xbfb8aa3b, v0
	v_exp_f32_e32 v0, v0
	v_pk_mul_f32 v[78:79], v[78:79], v[84:85]
	v_add_f32_e32 v0, 1.0, v0
	v_rcp_f32_e32 v84, v0
	v_mul_f32_e32 v0, 0x3d372713, v81
	v_mul_f32_e32 v0, v81, v0
	v_fma_f32 v0, v81, v0, v81
	v_mul_f32_e32 v0, 0x3fcc422a, v0
	v_mul_f32_e32 v0, 0xbfb8aa3b, v0
	v_exp_f32_e32 v0, v0
	s_nop 0
	v_add_f32_e32 v0, 1.0, v0
	v_rcp_f32_e32 v85, v0
	v_mul_f32_e32 v0, 0x3d372713, v74
	v_mul_f32_e32 v0, v74, v0
	v_fma_f32 v0, v74, v0, v74
	v_mul_f32_e32 v0, 0x3fcc422a, v0
	v_mul_f32_e32 v0, 0xbfb8aa3b, v0
	v_exp_f32_e32 v0, v0
	v_pk_mul_f32 v[80:81], v[80:81], v[84:85]
	v_add_f32_e32 v0, 1.0, v0
	v_rcp_f32_e32 v84, v0
	v_mul_f32_e32 v0, 0x3d372713, v75
	v_mul_f32_e32 v0, v75, v0
	v_fma_f32 v0, v75, v0, v75
	v_mul_f32_e32 v0, 0x3fcc422a, v0
	v_mul_f32_e32 v0, 0xbfb8aa3b, v0
	v_exp_f32_e32 v0, v0
	s_nop 0
	v_add_f32_e32 v0, 1.0, v0
	v_rcp_f32_e32 v85, v0
	s_nop 0
	v_pk_mul_f32 v[84:85], v[74:75], v[84:85]
	v_pk_add_f32 v[74:75], v[76:77], v[48:49]
	s_nop 0
	v_mul_f32_e32 v0, 0x3d372713, v74
	v_mul_f32_e32 v0, v74, v0
	v_fma_f32 v0, v74, v0, v74
	v_mul_f32_e32 v0, 0x3fcc422a, v0
	v_mul_f32_e32 v0, 0xbfb8aa3b, v0
	v_exp_f32_e32 v0, v0
	s_nop 0
	v_add_f32_e32 v0, 1.0, v0
	v_rcp_f32_e32 v76, v0
	v_mul_f32_e32 v0, 0x3d372713, v75
	v_mul_f32_e32 v0, v75, v0
	v_fma_f32 v0, v75, v0, v75
	v_mul_f32_e32 v0, 0x3fcc422a, v0
	v_mul_f32_e32 v0, 0xbfb8aa3b, v0
	v_exp_f32_e32 v0, v0
	s_nop 0
	v_add_f32_e32 v0, 1.0, v0
	v_rcp_f32_e32 v77, v0
	v_mul_f32_e32 v0, 0x3d372713, v70
	v_mul_f32_e32 v0, v70, v0
	v_fma_f32 v0, v70, v0, v70
	v_mul_f32_e32 v0, 0x3fcc422a, v0
	v_mul_f32_e32 v0, 0xbfb8aa3b, v0
	v_exp_f32_e32 v0, v0
	v_pk_mul_f32 v[86:87], v[74:75], v[76:77]
	v_cvt_pk_bf16_f32 v74, v78, v79
	v_add_co_u32_e32 v78, vcc, s6, v158
	v_cvt_pk_bf16_f32 v75, v80, v81
	v_cvt_pk_bf16_f32 v76, v84, v85
	v_cvt_pk_bf16_f32 v77, v86, v87
	v_addc_co_u32_e32 v79, vcc, 0, v159, vcc
	v_add_f32_e32 v0, 1.0, v0
	global_store_dwordx4 v[78:79], v[74:77], off
	s_mov_b64 s[6:7], 0x12000
	s_nop 0
	v_rcp_f32_e32 v74, v0
	v_mul_f32_e32 v0, 0x3d372713, v71
	v_mul_f32_e32 v0, v71, v0
	v_fma_f32 v0, v71, v0, v71
	v_mul_f32_e32 v0, 0x3fcc422a, v0
	v_mul_f32_e32 v0, 0xbfb8aa3b, v0
	v_exp_f32_e32 v0, v0
	s_nop 0
	v_add_f32_e32 v0, 1.0, v0
	v_rcp_f32_e32 v75, v0
	v_mul_f32_e32 v0, 0x3d372713, v72
	v_mul_f32_e32 v0, v72, v0
	v_fma_f32 v0, v72, v0, v72
	v_mul_f32_e32 v0, 0x3fcc422a, v0
	v_mul_f32_e32 v0, 0xbfb8aa3b, v0
	v_exp_f32_e32 v0, v0
	v_pk_mul_f32 v[70:71], v[70:71], v[74:75]
	v_add_f32_e32 v0, 1.0, v0
	v_rcp_f32_e32 v74, v0
	v_mul_f32_e32 v0, 0x3d372713, v73
	v_mul_f32_e32 v0, v73, v0
	v_fma_f32 v0, v73, v0, v73
	v_mul_f32_e32 v0, 0x3fcc422a, v0
	v_mul_f32_e32 v0, 0xbfb8aa3b, v0
	v_exp_f32_e32 v0, v0
	s_nop 0
	v_add_f32_e32 v0, 1.0, v0
	v_rcp_f32_e32 v75, v0
	v_mul_f32_e32 v0, 0x3d372713, v62
	v_mul_f32_e32 v0, v62, v0
	v_fma_f32 v0, v62, v0, v62
	v_mul_f32_e32 v0, 0x3fcc422a, v0
	v_mul_f32_e32 v0, 0xbfb8aa3b, v0
	v_exp_f32_e32 v0, v0
	v_pk_mul_f32 v[72:73], v[72:73], v[74:75]
	v_add_f32_e32 v0, 1.0, v0
	v_rcp_f32_e32 v74, v0
	v_mul_f32_e32 v0, 0x3d372713, v63
	v_mul_f32_e32 v0, v63, v0
	v_fma_f32 v0, v63, v0, v63
	v_mul_f32_e32 v0, 0x3fcc422a, v0
	v_mul_f32_e32 v0, 0xbfb8aa3b, v0
	v_exp_f32_e32 v0, v0
	s_nop 0
	v_add_f32_e32 v0, 1.0, v0
	v_rcp_f32_e32 v75, v0
	s_nop 0
	v_pk_mul_f32 v[74:75], v[62:63], v[74:75]
	v_pk_add_f32 v[62:63], v[64:65], v[40:41]
	s_nop 0
	v_mul_f32_e32 v0, 0x3d372713, v62
	v_mul_f32_e32 v0, v62, v0
	v_fma_f32 v0, v62, v0, v62
	v_mul_f32_e32 v0, 0x3fcc422a, v0
	v_mul_f32_e32 v0, 0xbfb8aa3b, v0
	v_exp_f32_e32 v0, v0
	s_nop 0
	v_add_f32_e32 v0, 1.0, v0
	v_rcp_f32_e32 v64, v0
	v_mul_f32_e32 v0, 0x3d372713, v63
	v_mul_f32_e32 v0, v63, v0
	v_fma_f32 v0, v63, v0, v63
	v_mul_f32_e32 v0, 0x3fcc422a, v0
	v_mul_f32_e32 v0, 0xbfb8aa3b, v0
	v_exp_f32_e32 v0, v0
	s_nop 0
	v_add_f32_e32 v0, 1.0, v0
	v_rcp_f32_e32 v65, v0
	v_mul_f32_e32 v0, 0x3d372713, v58
	v_mul_f32_e32 v0, v58, v0
	v_fma_f32 v0, v58, v0, v58
; __device__ __forceinline__ unsigned pk2(float lo, float hi) { const f32x2 f = {lo, hi}; const bf16n2 v = __builtin_convertvector(f, bf16n2); return __builtin_bit_cast(unsigned, v); }
; __device__ __forceinline__ float sigmoidf_(float x) { return __builtin_amdgcn_rcpf(1.0f + __expf(-x)); }
;     __device__ __forceinline__ bool operator()(f32x4 (&acc)[2][2][4][2], const Unit& u, int wr, int wc, int fr, int fq) const {
;     ...
;         for (int ai = 0; ai < 2; ++ai)
; #pragma unroll
;             for (int m = 0; m < 4; ++m) { bf16_t* rowp = hid + ((size_t)kv * 2048 + row0 + ai * HALF + m * 16) * 256 + col0;
; #pragma unroll
;                 for (int bj = 0; bj < 2; ++bj) { float o[8];
; #pragma unroll
;                     for (int j = 0; j < 8; ++j) { const float x = acc[ai][bj][m][j >> 2][j & 3] + bv[bj][j];
;                         o[j] = x * sigmoidf_(1.5957691216f * (x + 0.044715f * x * x * x)); }
;                     u32x4 w; w.x = pk2(o[0], o[1]); w.y = pk2(o[2], o[3]); w.z = pk2(o[4], o[5]); w.w = pk2(o[6], o[7]);
;                     *(u32x4*)(rowp + bj * HALF) = w; } }
	v_mul_f32_e32 v0, 0x3fcc422a, v0
	v_mul_f32_e32 v0, 0xbfb8aa3b, v0
	v_exp_f32_e32 v0, v0
	v_pk_mul_f32 v[76:77], v[62:63], v[64:65]
	v_cvt_pk_bf16_f32 v62, v70, v71
	v_cvt_pk_bf16_f32 v63, v72, v73
	v_cvt_pk_bf16_f32 v64, v74, v75
	v_cvt_pk_bf16_f32 v65, v76, v77
	v_add_f32_e32 v0, 1.0, v0
	global_store_dwordx4 v[82:83], v[62:65], off offset:256
	s_nop 1
	v_rcp_f32_e32 v64, v0
	v_mul_f32_e32 v0, 0x3d372713, v59
	v_mul_f32_e32 v0, v59, v0
	v_fma_f32 v0, v59, v0, v59
	v_mul_f32_e32 v0, 0x3fcc422a, v0
	v_mul_f32_e32 v0, 0xbfb8aa3b, v0
	v_exp_f32_e32 v0, v0
	v_lshl_add_u64 v[62:63], v[158:159], 0, s[6:7]
	s_mov_b32 s6, 0x12000
	v_add_f32_e32 v0, 1.0, v0
	v_rcp_f32_e32 v65, v0
	v_mul_f32_e32 v0, 0x3d372713, v60
	v_mul_f32_e32 v0, v60, v0
	v_fma_f32 v0, v60, v0, v60
	v_mul_f32_e32 v0, 0x3fcc422a, v0
	v_mul_f32_e32 v0, 0xbfb8aa3b, v0
	v_exp_f32_e32 v0, v0
	v_pk_mul_f32 v[58:59], v[58:59], v[64:65]
	v_add_f32_e32 v0, 1.0, v0
	v_rcp_f32_e32 v64, v0
	v_mul_f32_e32 v0, 0x3d372713, v61
	v_mul_f32_e32 v0, v61, v0
	v_fma_f32 v0, v61, v0, v61
	v_mul_f32_e32 v0, 0x3fcc422a, v0
	v_mul_f32_e32 v0, 0xbfb8aa3b, v0
	v_exp_f32_e32 v0, v0
	s_nop 0
	v_add_f32_e32 v0, 1.0, v0
	v_rcp_f32_e32 v65, v0
	v_mul_f32_e32 v0, 0x3d372713, v50
	v_mul_f32_e32 v0, v50, v0
	v_fma_f32 v0, v50, v0, v50
	v_mul_f32_e32 v0, 0x3fcc422a, v0
	v_mul_f32_e32 v0, 0xbfb8aa3b, v0
	v_exp_f32_e32 v0, v0
	v_pk_mul_f32 v[60:61], v[60:61], v[64:65]
	v_add_f32_e32 v0, 1.0, v0
	v_rcp_f32_e32 v64, v0
	v_mul_f32_e32 v0, 0x3d372713, v51
	v_mul_f32_e32 v0, v51, v0
	v_fma_f32 v0, v51, v0, v51
	v_mul_f32_e32 v0, 0x3fcc422a, v0
	v_mul_f32_e32 v0, 0xbfb8aa3b, v0
	v_exp_f32_e32 v0, v0
	s_nop 0
	v_add_f32_e32 v0, 1.0, v0
	v_rcp_f32_e32 v65, v0
	s_nop 0
	v_pk_mul_f32 v[64:65], v[50:51], v[64:65]
	v_pk_add_f32 v[50:51], v[52:53], v[48:49]
	s_nop 0
	v_mul_f32_e32 v0, 0x3d372713, v50
	v_mul_f32_e32 v0, v50, v0
	v_fma_f32 v0, v50, v0, v50
	v_mul_f32_e32 v0, 0x3fcc422a, v0
	v_mul_f32_e32 v0, 0xbfb8aa3b, v0
	v_exp_f32_e32 v0, v0
	s_nop 0
	v_add_f32_e32 v0, 1.0, v0
	v_rcp_f32_e32 v52, v0
	v_mul_f32_e32 v0, 0x3d372713, v51
	v_mul_f32_e32 v0, v51, v0
	v_fma_f32 v0, v51, v0, v51
	v_mul_f32_e32 v0, 0x3fcc422a, v0
	v_mul_f32_e32 v0, 0xbfb8aa3b, v0
	v_exp_f32_e32 v0, v0
	s_nop 0
	v_add_f32_e32 v0, 1.0, v0
	v_rcp_f32_e32 v53, v0
	v_mul_f32_e32 v0, 0x3d372713, v42
	v_mul_f32_e32 v0, v42, v0
	v_fma_f32 v0, v42, v0, v42
	v_mul_f32_e32 v0, 0x3fcc422a, v0
	v_mul_f32_e32 v0, 0xbfb8aa3b, v0
	v_exp_f32_e32 v0, v0
	v_pk_mul_f32 v[70:71], v[50:51], v[52:53]
	v_cvt_pk_bf16_f32 v50, v58, v59
	v_add_co_u32_e32 v58, vcc, s6, v158
	v_cvt_pk_bf16_f32 v51, v60, v61
	v_cvt_pk_bf16_f32 v52, v64, v65
	v_cvt_pk_bf16_f32 v53, v70, v71
	v_addc_co_u32_e32 v59, vcc, 0, v159, vcc
	v_add_f32_e32 v0, 1.0, v0
	global_store_dwordx4 v[58:59], v[50:53], off
	s_mov_b64 s[6:7], 0x14000
	s_nop 0
	v_rcp_f32_e32 v50, v0
	v_mul_f32_e32 v0, 0x3d372713, v43
	v_mul_f32_e32 v0, v43, v0
	v_fma_f32 v0, v43, v0, v43
	v_mul_f32_e32 v0, 0x3fcc422a, v0
	v_mul_f32_e32 v0, 0xbfb8aa3b, v0
	v_exp_f32_e32 v0, v0
	s_nop 0
	v_add_f32_e32 v0, 1.0, v0
	v_rcp_f32_e32 v51, v0
	v_mul_f32_e32 v0, 0x3d372713, v44
	v_mul_f32_e32 v0, v44, v0
	v_fma_f32 v0, v44, v0, v44
	v_mul_f32_e32 v0, 0x3fcc422a, v0
	v_mul_f32_e32 v0, 0xbfb8aa3b, v0
	v_exp_f32_e32 v0, v0
	v_pk_mul_f32 v[42:43], v[42:43], v[50:51]
	v_add_f32_e32 v0, 1.0, v0
	v_rcp_f32_e32 v50, v0
	v_mul_f32_e32 v0, 0x3d372713, v45
	v_mul_f32_e32 v0, v45, v0
	v_fma_f32 v0, v45, v0, v45
	v_mul_f32_e32 v0, 0x3fcc422a, v0
	v_mul_f32_e32 v0, 0xbfb8aa3b, v0
	v_exp_f32_e32 v0, v0
	s_nop 0
	v_add_f32_e32 v0, 1.0, v0
	v_rcp_f32_e32 v51, v0
	v_mul_f32_e32 v0, 0x3d372713, v34
	v_mul_f32_e32 v0, v34, v0
	v_fma_f32 v0, v34, v0, v34
	v_mul_f32_e32 v0, 0x3fcc422a, v0
	v_mul_f32_e32 v0, 0xbfb8aa3b, v0
	v_exp_f32_e32 v0, v0
	v_pk_mul_f32 v[44:45], v[44:45], v[50:51]
	v_add_f32_e32 v0, 1.0, v0
	v_rcp_f32_e32 v50, v0
	v_mul_f32_e32 v0, 0x3d372713, v35
	v_mul_f32_e32 v0, v35, v0
	v_fma_f32 v0, v35, v0, v35
	v_mul_f32_e32 v0, 0x3fcc422a, v0
	v_mul_f32_e32 v0, 0xbfb8aa3b, v0
	v_exp_f32_e32 v0, v0
	s_nop 0
	v_add_f32_e32 v0, 1.0, v0
	v_rcp_f32_e32 v51, v0
	s_nop 0
	v_pk_mul_f32 v[50:51], v[34:35], v[50:51]
	v_pk_add_f32 v[34:35], v[36:37], v[40:41]
	s_nop 0
	v_mul_f32_e32 v0, 0x3d372713, v34
	v_mul_f32_e32 v0, v34, v0
	v_fma_f32 v0, v34, v0, v34
	v_mul_f32_e32 v0, 0x3fcc422a, v0
	v_mul_f32_e32 v0, 0xbfb8aa3b, v0
	v_exp_f32_e32 v0, v0
	s_nop 0
	v_add_f32_e32 v0, 1.0, v0
	v_rcp_f32_e32 v36, v0
	v_mul_f32_e32 v0, 0x3d372713, v35
	v_mul_f32_e32 v0, v35, v0
	v_fma_f32 v0, v35, v0, v35
	v_mul_f32_e32 v0, 0x3fcc422a, v0
	v_mul_f32_e32 v0, 0xbfb8aa3b, v0
	v_exp_f32_e32 v0, v0
	s_nop 0
	v_add_f32_e32 v0, 1.0, v0
	v_rcp_f32_e32 v37, v0
	v_mul_f32_e32 v0, 0x3d372713, v30
	v_mul_f32_e32 v0, v30, v0
	v_fma_f32 v0, v30, v0, v30
	v_mul_f32_e32 v0, 0x3fcc422a, v0
	v_mul_f32_e32 v0, 0xbfb8aa3b, v0
	v_exp_f32_e32 v0, v0
	v_pk_mul_f32 v[52:53], v[34:35], v[36:37]
	v_cvt_pk_bf16_f32 v34, v42, v43
	v_cvt_pk_bf16_f32 v35, v44, v45
	v_cvt_pk_bf16_f32 v36, v50, v51
	v_cvt_pk_bf16_f32 v37, v52, v53
	v_add_f32_e32 v0, 1.0, v0
	global_store_dwordx4 v[62:63], v[34:37], off offset:256
	s_nop 1
	v_rcp_f32_e32 v36, v0
	v_mul_f32_e32 v0, 0x3d372713, v31
	v_mul_f32_e32 v0, v31, v0
	v_fma_f32 v0, v31, v0, v31
	v_mul_f32_e32 v0, 0x3fcc422a, v0
	v_mul_f32_e32 v0, 0xbfb8aa3b, v0
	v_exp_f32_e32 v0, v0
	v_lshl_add_u64 v[34:35], v[158:159], 0, s[6:7]
	s_mov_b32 s6, 0x14000
	v_add_f32_e32 v0, 1.0, v0
	v_rcp_f32_e32 v37, v0
	v_mul_f32_e32 v0, 0x3d372713, v32
	v_mul_f32_e32 v0, v32, v0
	v_fma_f32 v0, v32, v0, v32
	v_mul_f32_e32 v0, 0x3fcc422a, v0
	v_mul_f32_e32 v0, 0xbfb8aa3b, v0
; __device__ __forceinline__ unsigned pk2(float lo, float hi) { const f32x2 f = {lo, hi}; const bf16n2 v = __builtin_convertvector(f, bf16n2); return __builtin_bit_cast(unsigned, v); }
; __device__ __forceinline__ float sigmoidf_(float x) { return __builtin_amdgcn_rcpf(1.0f + __expf(-x)); }
;     __device__ __forceinline__ bool operator()(f32x4 (&acc)[2][2][4][2], const Unit& u, int wr, int wc, int fr, int fq) const {
;     ...
;         for (int ai = 0; ai < 2; ++ai)
; #pragma unroll
;             for (int m = 0; m < 4; ++m) { bf16_t* rowp = hid + ((size_t)kv * 2048 + row0 + ai * HALF + m * 16) * 256 + col0;
; #pragma unroll
;                 for (int bj = 0; bj < 2; ++bj) { float o[8];
; #pragma unroll
;                     for (int j = 0; j < 8; ++j) { const float x = acc[ai][bj][m][j >> 2][j & 3] + bv[bj][j];
;                         o[j] = x * sigmoidf_(1.5957691216f * (x + 0.044715f * x * x * x)); }
;                     u32x4 w; w.x = pk2(o[0], o[1]); w.y = pk2(o[2], o[3]); w.z = pk2(o[4], o[5]); w.w = pk2(o[6], o[7]);
;                     *(u32x4*)(rowp + bj * HALF) = w; } }
	v_exp_f32_e32 v0, v0
	v_pk_mul_f32 v[30:31], v[30:31], v[36:37]
	v_add_f32_e32 v0, 1.0, v0
	v_rcp_f32_e32 v36, v0
	v_mul_f32_e32 v0, 0x3d372713, v33
	v_mul_f32_e32 v0, v33, v0
	v_fma_f32 v0, v33, v0, v33
	v_mul_f32_e32 v0, 0x3fcc422a, v0
	v_mul_f32_e32 v0, 0xbfb8aa3b, v0
	v_exp_f32_e32 v0, v0
	s_nop 0
	v_add_f32_e32 v0, 1.0, v0
	v_rcp_f32_e32 v37, v0
	v_mul_f32_e32 v0, 0x3d372713, v26
	v_mul_f32_e32 v0, v26, v0
	v_fma_f32 v0, v26, v0, v26
	v_mul_f32_e32 v0, 0x3fcc422a, v0
	v_mul_f32_e32 v0, 0xbfb8aa3b, v0
	v_exp_f32_e32 v0, v0
	v_pk_mul_f32 v[32:33], v[32:33], v[36:37]
	v_add_f32_e32 v0, 1.0, v0
	v_rcp_f32_e32 v36, v0
	v_mul_f32_e32 v0, 0x3d372713, v27
	v_mul_f32_e32 v0, v27, v0
	v_fma_f32 v0, v27, v0, v27
	v_mul_f32_e32 v0, 0x3fcc422a, v0
	v_mul_f32_e32 v0, 0xbfb8aa3b, v0
	v_exp_f32_e32 v0, v0
	s_nop 0
	v_add_f32_e32 v0, 1.0, v0
	v_rcp_f32_e32 v37, v0
	s_nop 0
	v_pk_mul_f32 v[36:37], v[26:27], v[36:37]
	v_pk_add_f32 v[26:27], v[28:29], v[48:49]
	s_nop 0
	v_mul_f32_e32 v0, 0x3d372713, v26
	v_mul_f32_e32 v0, v26, v0
	v_fma_f32 v0, v26, v0, v26
	v_mul_f32_e32 v0, 0x3fcc422a, v0
	v_mul_f32_e32 v0, 0xbfb8aa3b, v0
	v_exp_f32_e32 v0, v0
	s_nop 0
	v_add_f32_e32 v0, 1.0, v0
	v_rcp_f32_e32 v28, v0
	v_mul_f32_e32 v0, 0x3d372713, v27
	v_mul_f32_e32 v0, v27, v0
	v_fma_f32 v0, v27, v0, v27
	v_mul_f32_e32 v0, 0x3fcc422a, v0
	v_mul_f32_e32 v0, 0xbfb8aa3b, v0
	v_exp_f32_e32 v0, v0
	s_nop 0
	v_add_f32_e32 v0, 1.0, v0
	v_rcp_f32_e32 v29, v0
	v_mul_f32_e32 v0, 0x3d372713, v22
	v_mul_f32_e32 v0, v22, v0
	v_fma_f32 v0, v22, v0, v22
	v_mul_f32_e32 v0, 0x3fcc422a, v0
	v_mul_f32_e32 v0, 0xbfb8aa3b, v0
	v_exp_f32_e32 v0, v0
	v_pk_mul_f32 v[42:43], v[26:27], v[28:29]
	v_cvt_pk_bf16_f32 v26, v30, v31
	v_add_co_u32_e32 v30, vcc, s6, v158
	v_cvt_pk_bf16_f32 v27, v32, v33
	v_cvt_pk_bf16_f32 v28, v36, v37
	v_cvt_pk_bf16_f32 v29, v42, v43
	v_addc_co_u32_e32 v31, vcc, 0, v159, vcc
	v_add_f32_e32 v0, 1.0, v0
	global_store_dwordx4 v[30:31], v[26:29], off
	s_mov_b64 s[6:7], 0x16000
	s_nop 0
	v_rcp_f32_e32 v26, v0
	v_mul_f32_e32 v0, 0x3d372713, v23
	v_mul_f32_e32 v0, v23, v0
	v_fma_f32 v0, v23, v0, v23
	v_mul_f32_e32 v0, 0x3fcc422a, v0
	v_mul_f32_e32 v0, 0xbfb8aa3b, v0
	v_exp_f32_e32 v0, v0
	s_nop 0
	v_add_f32_e32 v0, 1.0, v0
	v_rcp_f32_e32 v27, v0
	v_mul_f32_e32 v0, 0x3d372713, v24
	v_mul_f32_e32 v0, v24, v0
	v_fma_f32 v0, v24, v0, v24
	v_mul_f32_e32 v0, 0x3fcc422a, v0
	v_mul_f32_e32 v0, 0xbfb8aa3b, v0
	v_exp_f32_e32 v0, v0
	v_pk_mul_f32 v[22:23], v[22:23], v[26:27]
	v_add_f32_e32 v0, 1.0, v0
	v_rcp_f32_e32 v26, v0
	v_mul_f32_e32 v0, 0x3d372713, v25
	v_mul_f32_e32 v0, v25, v0
	v_fma_f32 v0, v25, v0, v25
	v_mul_f32_e32 v0, 0x3fcc422a, v0
	v_mul_f32_e32 v0, 0xbfb8aa3b, v0
	v_exp_f32_e32 v0, v0
	s_nop 0
	v_add_f32_e32 v0, 1.0, v0
	v_rcp_f32_e32 v27, v0
	v_mul_f32_e32 v0, 0x3d372713, v18
	v_mul_f32_e32 v0, v18, v0
	v_fma_f32 v0, v18, v0, v18
	v_mul_f32_e32 v0, 0x3fcc422a, v0
	v_mul_f32_e32 v0, 0xbfb8aa3b, v0
	v_exp_f32_e32 v0, v0
	v_pk_mul_f32 v[24:25], v[24:25], v[26:27]
	v_add_f32_e32 v0, 1.0, v0
	v_rcp_f32_e32 v26, v0
	v_mul_f32_e32 v0, 0x3d372713, v19
	v_mul_f32_e32 v0, v19, v0
	v_fma_f32 v0, v19, v0, v19
	v_mul_f32_e32 v0, 0x3fcc422a, v0
	v_mul_f32_e32 v0, 0xbfb8aa3b, v0
	v_exp_f32_e32 v0, v0
	s_nop 0
	v_add_f32_e32 v0, 1.0, v0
	v_rcp_f32_e32 v27, v0
	s_nop 0
	v_pk_mul_f32 v[26:27], v[18:19], v[26:27]
	v_pk_add_f32 v[18:19], v[20:21], v[40:41]
	s_nop 0
	v_mul_f32_e32 v0, 0x3d372713, v18
	v_mul_f32_e32 v0, v18, v0
	v_fma_f32 v0, v18, v0, v18
	v_mul_f32_e32 v0, 0x3fcc422a, v0
	v_mul_f32_e32 v0, 0xbfb8aa3b, v0
	v_exp_f32_e32 v0, v0
	s_nop 0
	v_add_f32_e32 v0, 1.0, v0
	v_rcp_f32_e32 v20, v0
	v_mul_f32_e32 v0, 0x3d372713, v19
	v_mul_f32_e32 v0, v19, v0
	v_fma_f32 v0, v19, v0, v19
	v_mul_f32_e32 v0, 0x3fcc422a, v0
	v_mul_f32_e32 v0, 0xbfb8aa3b, v0
	v_exp_f32_e32 v0, v0
	s_nop 0
	v_add_f32_e32 v0, 1.0, v0
	v_rcp_f32_e32 v21, v0
	v_mul_f32_e32 v0, 0x3d372713, v14
	v_mul_f32_e32 v0, v14, v0
	v_fma_f32 v0, v14, v0, v14
	v_mul_f32_e32 v0, 0x3fcc422a, v0
	v_mul_f32_e32 v0, 0xbfb8aa3b, v0
	v_exp_f32_e32 v0, v0
	v_pk_mul_f32 v[28:29], v[18:19], v[20:21]
	v_cvt_pk_bf16_f32 v18, v22, v23
	v_cvt_pk_bf16_f32 v19, v24, v25
	v_cvt_pk_bf16_f32 v20, v26, v27
	v_cvt_pk_bf16_f32 v21, v28, v29
	v_add_f32_e32 v0, 1.0, v0
	global_store_dwordx4 v[34:35], v[18:21], off offset:256
	s_nop 1
	v_rcp_f32_e32 v20, v0
	v_mul_f32_e32 v0, 0x3d372713, v15
	v_mul_f32_e32 v0, v15, v0
	v_fma_f32 v0, v15, v0, v15
; __device__ __forceinline__ unsigned pk2(float lo, float hi) { const f32x2 f = {lo, hi}; const bf16n2 v = __builtin_convertvector(f, bf16n2); return __builtin_bit_cast(unsigned, v); }
; __device__ __forceinline__ float sigmoidf_(float x) { return __builtin_amdgcn_rcpf(1.0f + __expf(-x)); }
;     __device__ __forceinline__ bool operator()(f32x4 (&acc)[2][2][4][2], const Unit& u, int wr, int wc, int fr, int fq) const {
;     ...
;         for (int ai = 0; ai < 2; ++ai)
; #pragma unroll
;             for (int m = 0; m < 4; ++m) { bf16_t* rowp = hid + ((size_t)kv * 2048 + row0 + ai * HALF + m * 16) * 256 + col0;
; #pragma unroll
;                 for (int bj = 0; bj < 2; ++bj) { float o[8];
; #pragma unroll
;                     for (int j = 0; j < 8; ++j) { const float x = acc[ai][bj][m][j >> 2][j & 3] + bv[bj][j];
;                         o[j] = x * sigmoidf_(1.5957691216f * (x + 0.044715f * x * x * x)); }
;                     u32x4 w; w.x = pk2(o[0], o[1]); w.y = pk2(o[2], o[3]); w.z = pk2(o[4], o[5]); w.w = pk2(o[6], o[7]);
;                     *(u32x4*)(rowp + bj * HALF) = w; } }
;         return false;
;     }
	v_mul_f32_e32 v0, 0x3fcc422a, v0
	v_mul_f32_e32 v0, 0xbfb8aa3b, v0
	v_exp_f32_e32 v0, v0
	v_lshl_add_u64 v[18:19], v[158:159], 0, s[6:7]
	s_mov_b32 s6, 0x16000
	v_add_f32_e32 v0, 1.0, v0
	v_rcp_f32_e32 v21, v0
	v_mul_f32_e32 v0, 0x3d372713, v16
	v_mul_f32_e32 v0, v16, v0
	v_fma_f32 v0, v16, v0, v16
	v_mul_f32_e32 v0, 0x3fcc422a, v0
	v_mul_f32_e32 v0, 0xbfb8aa3b, v0
	v_exp_f32_e32 v0, v0
	v_pk_mul_f32 v[14:15], v[14:15], v[20:21]
	v_add_f32_e32 v0, 1.0, v0
	v_rcp_f32_e32 v20, v0
	v_mul_f32_e32 v0, 0x3d372713, v17
	v_mul_f32_e32 v0, v17, v0
	v_fma_f32 v0, v17, v0, v17
	v_mul_f32_e32 v0, 0x3fcc422a, v0
	v_mul_f32_e32 v0, 0xbfb8aa3b, v0
	v_exp_f32_e32 v0, v0
	s_nop 0
	v_add_f32_e32 v0, 1.0, v0
	v_rcp_f32_e32 v21, v0
	v_mul_f32_e32 v0, 0x3d372713, v10
	v_mul_f32_e32 v0, v10, v0
	v_fma_f32 v0, v10, v0, v10
	v_mul_f32_e32 v0, 0x3fcc422a, v0
	v_mul_f32_e32 v0, 0xbfb8aa3b, v0
	v_exp_f32_e32 v0, v0
	v_pk_mul_f32 v[16:17], v[16:17], v[20:21]
	v_add_f32_e32 v0, 1.0, v0
	v_rcp_f32_e32 v20, v0
	v_mul_f32_e32 v0, 0x3d372713, v11
	v_mul_f32_e32 v0, v11, v0
	v_fma_f32 v0, v11, v0, v11
	v_mul_f32_e32 v0, 0x3fcc422a, v0
	v_mul_f32_e32 v0, 0xbfb8aa3b, v0
	v_exp_f32_e32 v0, v0
	s_nop 0
	v_add_f32_e32 v0, 1.0, v0
	v_rcp_f32_e32 v21, v0
	s_nop 0
	v_pk_mul_f32 v[20:21], v[10:11], v[20:21]
	v_pk_add_f32 v[10:11], v[12:13], v[48:49]
	s_nop 0
	v_mul_f32_e32 v0, 0x3d372713, v10
	v_mul_f32_e32 v0, v10, v0
	v_fma_f32 v0, v10, v0, v10
	v_mul_f32_e32 v0, 0x3fcc422a, v0
	v_mul_f32_e32 v0, 0xbfb8aa3b, v0
	v_exp_f32_e32 v0, v0
	s_nop 0
	v_add_f32_e32 v0, 1.0, v0
	v_rcp_f32_e32 v12, v0
	v_mul_f32_e32 v0, 0x3d372713, v11
	v_mul_f32_e32 v0, v11, v0
	v_fma_f32 v0, v11, v0, v11
	v_mul_f32_e32 v0, 0x3fcc422a, v0
	v_mul_f32_e32 v0, 0xbfb8aa3b, v0
	v_exp_f32_e32 v0, v0
	s_nop 0
	v_add_f32_e32 v0, 1.0, v0
	v_rcp_f32_e32 v13, v0
	v_mul_f32_e32 v0, 0x3d372713, v6
	v_mul_f32_e32 v0, v6, v0
	v_fma_f32 v0, v6, v0, v6
	v_mul_f32_e32 v0, 0x3fcc422a, v0
	v_mul_f32_e32 v0, 0xbfb8aa3b, v0
	v_exp_f32_e32 v0, v0
	v_pk_mul_f32 v[22:23], v[10:11], v[12:13]
	v_cvt_pk_bf16_f32 v10, v14, v15
	v_add_co_u32_e32 v14, vcc, s6, v158
	v_cvt_pk_bf16_f32 v11, v16, v17
	v_cvt_pk_bf16_f32 v12, v20, v21
	v_cvt_pk_bf16_f32 v13, v22, v23
	v_addc_co_u32_e32 v15, vcc, 0, v159, vcc
	v_add_f32_e32 v0, 1.0, v0
	global_store_dwordx4 v[14:15], v[10:13], off
	s_and_b64 vcc, exec, s[0:1]
	s_mov_b64 s[6:7], s[4:5]
	v_rcp_f32_e32 v10, v0
	v_mul_f32_e32 v0, 0x3d372713, v7
	v_mul_f32_e32 v0, v7, v0
	v_fma_f32 v0, v7, v0, v7
	v_mul_f32_e32 v0, 0x3fcc422a, v0
	v_mul_f32_e32 v0, 0xbfb8aa3b, v0
	v_exp_f32_e32 v0, v0
	s_nop 0
	v_add_f32_e32 v0, 1.0, v0
	v_rcp_f32_e32 v11, v0
	v_mul_f32_e32 v0, 0x3d372713, v8
	v_mul_f32_e32 v0, v8, v0
	v_fma_f32 v0, v8, v0, v8
	v_mul_f32_e32 v0, 0x3fcc422a, v0
	v_mul_f32_e32 v0, 0xbfb8aa3b, v0
	v_exp_f32_e32 v0, v0
	v_pk_mul_f32 v[6:7], v[6:7], v[10:11]
	v_add_f32_e32 v0, 1.0, v0
	v_rcp_f32_e32 v10, v0
	v_mul_f32_e32 v0, 0x3d372713, v9
	v_mul_f32_e32 v0, v9, v0
	v_fma_f32 v0, v9, v0, v9
	v_mul_f32_e32 v0, 0x3fcc422a, v0
	v_mul_f32_e32 v0, 0xbfb8aa3b, v0
	v_exp_f32_e32 v0, v0
	s_nop 0
	v_add_f32_e32 v0, 1.0, v0
	v_rcp_f32_e32 v11, v0
	v_mul_f32_e32 v0, 0x3d372713, v2
	v_mul_f32_e32 v0, v2, v0
	v_fma_f32 v0, v2, v0, v2
	v_mul_f32_e32 v0, 0x3fcc422a, v0
	v_mul_f32_e32 v0, 0xbfb8aa3b, v0
	v_exp_f32_e32 v0, v0
	v_pk_mul_f32 v[8:9], v[8:9], v[10:11]
	v_add_f32_e32 v0, 1.0, v0
	v_rcp_f32_e32 v10, v0
	v_mul_f32_e32 v0, 0x3d372713, v3
	v_mul_f32_e32 v0, v3, v0
	v_fma_f32 v0, v3, v0, v3
	v_mul_f32_e32 v0, 0x3fcc422a, v0
	v_mul_f32_e32 v0, 0xbfb8aa3b, v0
	v_exp_f32_e32 v0, v0
	s_nop 0
	v_add_f32_e32 v0, 1.0, v0
	v_rcp_f32_e32 v11, v0
	s_nop 0
	v_pk_mul_f32 v[10:11], v[2:3], v[10:11]
	v_pk_add_f32 v[2:3], v[4:5], v[40:41]
	s_nop 0
	v_mul_f32_e32 v0, 0x3d372713, v2
	v_mul_f32_e32 v0, v2, v0
	v_fma_f32 v0, v2, v0, v2
	v_mul_f32_e32 v0, 0x3fcc422a, v0
	v_mul_f32_e32 v0, 0xbfb8aa3b, v0
	v_exp_f32_e32 v0, v0
	s_nop 0
	v_add_f32_e32 v0, 1.0, v0
	v_rcp_f32_e32 v4, v0
	v_mul_f32_e32 v0, 0x3d372713, v3
	v_mul_f32_e32 v0, v3, v0
	v_fma_f32 v0, v3, v0, v3
	v_mul_f32_e32 v0, 0x3fcc422a, v0
	v_mul_f32_e32 v0, 0xbfb8aa3b, v0
	v_exp_f32_e32 v0, v0
	s_nop 0
	v_add_f32_e32 v0, 1.0, v0
	v_rcp_f32_e32 v5, v0
	s_nop 0
	v_pk_mul_f32 v[12:13], v[2:3], v[4:5]
	v_cvt_pk_bf16_f32 v2, v6, v7
	v_cvt_pk_bf16_f32 v3, v8, v9
	v_cvt_pk_bf16_f32 v4, v10, v11
	v_cvt_pk_bf16_f32 v5, v12, v13
	global_store_dwordx4 v[18:19], v[2:5], off offset:256
	s_cbranch_vccz .LBB0_482
